# nt (streaming) hint on the in-proj0 GEMM epilogue stores and conversion-hook stores in P2, so the write-once outputs do not displace the A/B panels in L2
# speedup vs baseline: 1.0075x; 1.0061x over previous
; #define LAS __attribute__((address_space(3)))
; __device__ __forceinline__ int opaque_tid() { int t = threadIdx.x; asm volatile("" : "+v"(t)); return t; }
; __device__ __forceinline__ unsigned pk2(float a, float b) { f32x2 v = {a, b}; bf16x2_t r = __builtin_convertvector(v, bf16x2_t); return __builtin_bit_cast(unsigned, r); }
;     __device__ __forceinline__ void operator()(int ui) { if (ui == slot) run(); }
;     __device__ __forceinline__ void run() { done = true;
;         const int tid_ = opaque_tid(), wave = tid_ >> 6, lane = tid_ & 63;
;         if (wave < 7) { LAS unsigned* scr = (LAS unsigned*)(lds + 131072) + wave * (64 * 17);
;             for (int v = (int)blockIdx.x * 7 + wave; v < cv::N_GW + cv::I_IN1 + cv::I_OUT; v += (int)gridDim.x * 7) conv_dispatch(*p, v < cv::N_GW ? cv::I_IN0 + cv::I_OUT + v : cv::I_L0 + (v - cv::N_GW), scr, lane); } }
;     __device__ __forceinline__ void operator()(const f32x4 (&acc)[2][2][4][2], const Unit& u, int wr, int wc, int fr, int fq) const {
;         const int row0 = u.pm * BM + wr * 64 + fr, col0 = u.pn * BM + wc * 32 + 8 * fq;
; #pragma unroll
;         for (int ai = 0; ai < 2; ++ai)
; #pragma unroll
;             for (int m = 0; m < 4; ++m) { bf16_t* rowp = O + (size_t)(row0 + ai * HALF + m * 16) * ldc + col0;
; #pragma unroll
;                 for (int bj = 0; bj < 2; ++bj) { const f32x4 v0 = acc[ai][bj][m][0] * sc, v1 = acc[ai][bj][m][1] * sc;
;                     u32x4 w; w.x = pk2(v0[0], v0[1]); w.y = pk2(v0[2], v0[3]); w.z = pk2(v1[0], v1[1]); w.w = pk2(v1[2], v1[3]);
;                     *(u32x4*)(rowp + bj * HALF) = w; } }
.LBB0_153:
	v_mov_b32_e32 v0, v241
	s_nop 15
	s_nop 7
	s_lshl_b32 s8, s8, 8
	v_readfirstlane_b32 s37, v0
	s_ashr_i32 s39, s37, 2
	s_andn2_b32 s39, s39, 63
	s_lshr_b32 s37, s37, 1
	s_add_i32 s39, s39, s8
	s_lshl_b32 s8, s50, 8
	s_and_b32 s37, s37, 0x60
	v_and_or_b32 v16, v0, 15, s39
	s_or_b32 s8, s37, s8
	v_lshrrev_b32_e32 v0, 1, v0
	v_and_or_b32 v4, v0, 24, s8
	v_ashrrev_i32_e32 v5, 31, v4
	v_mov_b64_e32 v[2:3], s[22:23]
	v_mad_i64_i32 v[6:7], s[44:45], v16, s65, v[2:3]
	v_lshlrev_b64 v[4:5], 1, v[4:5]
	v_lshl_add_u64 v[10:11], v[6:7], 0, v[4:5]
	v_pk_mul_f32 v[8:9], v[160:161], s[18:19] op_sel_hi:[1,0]
	v_pk_mul_f32 v[6:7], v[158:159], s[18:19] op_sel_hi:[1,0]
	v_pk_mul_f32 v[12:13], v[156:157], s[18:19] op_sel_hi:[1,0]
	v_pk_mul_f32 v[14:15], v[154:155], s[18:19] op_sel_hi:[1,0]
	v_cvt_pk_bf16_f32 v6, v6, v7
	v_cvt_pk_bf16_f32 v7, v8, v9
	v_cvt_pk_bf16_f32 v8, v14, v15
	v_cvt_pk_bf16_f32 v9, v12, v13
	global_store_dwordx4 v[10:11], v[6:9], off nt
	v_pk_mul_f32 v[12:13], v[140:141], s[18:19] op_sel_hi:[1,0]
	v_pk_mul_f32 v[14:15], v[138:139], s[18:19] op_sel_hi:[1,0]
	v_pk_mul_f32 v[8:9], v[148:149], s[18:19] op_sel_hi:[1,0]
	v_pk_mul_f32 v[6:7], v[146:147], s[18:19] op_sel_hi:[1,0]
	v_or_b32_e32 v0, 16, v16
	v_cvt_pk_bf16_f32 v6, v6, v7
	v_cvt_pk_bf16_f32 v7, v8, v9
	v_cvt_pk_bf16_f32 v8, v14, v15
	v_cvt_pk_bf16_f32 v9, v12, v13
	global_store_dwordx4 v[10:11], v[6:9], off offset:256 nt
	v_pk_mul_f32 v[12:13], v[144:145], s[18:19] op_sel_hi:[1,0]
	v_pk_mul_f32 v[14:15], v[142:143], s[18:19] op_sel_hi:[1,0]
	v_mad_i64_i32 v[6:7], s[44:45], v0, s65, v[2:3]
	v_lshl_add_u64 v[10:11], v[6:7], 0, v[4:5]
	v_pk_mul_f32 v[8:9], v[152:153], s[18:19] op_sel_hi:[1,0]
	v_pk_mul_f32 v[6:7], v[150:151], s[18:19] op_sel_hi:[1,0]
	v_or_b32_e32 v0, 32, v16
	v_cvt_pk_bf16_f32 v6, v6, v7
	v_cvt_pk_bf16_f32 v7, v8, v9
	v_cvt_pk_bf16_f32 v8, v14, v15
	v_cvt_pk_bf16_f32 v9, v12, v13
	global_store_dwordx4 v[10:11], v[6:9], off nt
	v_pk_mul_f32 v[12:13], v[124:125], s[18:19] op_sel_hi:[1,0]
	v_pk_mul_f32 v[14:15], v[122:123], s[18:19] op_sel_hi:[1,0]
	v_pk_mul_f32 v[8:9], v[132:133], s[18:19] op_sel_hi:[1,0]
	v_pk_mul_f32 v[6:7], v[130:131], s[18:19] op_sel_hi:[1,0]
	s_cmp_lg_u32 s9, s58
	v_cvt_pk_bf16_f32 v6, v6, v7
	v_cvt_pk_bf16_f32 v7, v8, v9
	v_cvt_pk_bf16_f32 v8, v14, v15
	v_cvt_pk_bf16_f32 v9, v12, v13
	global_store_dwordx4 v[10:11], v[6:9], off offset:256 nt
	v_pk_mul_f32 v[12:13], v[128:129], s[18:19] op_sel_hi:[1,0]
	v_pk_mul_f32 v[14:15], v[126:127], s[18:19] op_sel_hi:[1,0]
	v_mad_i64_i32 v[6:7], s[44:45], v0, s65, v[2:3]
	v_lshl_add_u64 v[10:11], v[6:7], 0, v[4:5]
	v_pk_mul_f32 v[8:9], v[136:137], s[18:19] op_sel_hi:[1,0]
	v_pk_mul_f32 v[6:7], v[134:135], s[18:19] op_sel_hi:[1,0]
	v_or_b32_e32 v0, 48, v16
	v_cvt_pk_bf16_f32 v6, v6, v7
	v_cvt_pk_bf16_f32 v7, v8, v9
	v_cvt_pk_bf16_f32 v8, v14, v15
	v_cvt_pk_bf16_f32 v9, v12, v13
	global_store_dwordx4 v[10:11], v[6:9], off nt
	v_pk_mul_f32 v[12:13], v[108:109], s[18:19] op_sel_hi:[1,0]
	v_pk_mul_f32 v[14:15], v[106:107], s[18:19] op_sel_hi:[1,0]
	v_pk_mul_f32 v[8:9], v[116:117], s[18:19] op_sel_hi:[1,0]
	v_pk_mul_f32 v[6:7], v[114:115], s[18:19] op_sel_hi:[1,0]
	s_nop 0
	v_cvt_pk_bf16_f32 v6, v6, v7
	v_cvt_pk_bf16_f32 v7, v8, v9
	v_cvt_pk_bf16_f32 v8, v14, v15
	v_cvt_pk_bf16_f32 v9, v12, v13
	global_store_dwordx4 v[10:11], v[6:9], off offset:256 nt
	v_pk_mul_f32 v[12:13], v[112:113], s[18:19] op_sel_hi:[1,0]
	v_pk_mul_f32 v[14:15], v[110:111], s[18:19] op_sel_hi:[1,0]
	v_mad_i64_i32 v[6:7], s[44:45], v0, s65, v[2:3]
	v_lshl_add_u64 v[10:11], v[6:7], 0, v[4:5]
	v_pk_mul_f32 v[8:9], v[120:121], s[18:19] op_sel_hi:[1,0]
	v_pk_mul_f32 v[6:7], v[118:119], s[18:19] op_sel_hi:[1,0]
	v_add_u32_e32 v0, 0x80, v16
	v_cvt_pk_bf16_f32 v6, v6, v7
	v_cvt_pk_bf16_f32 v7, v8, v9
	v_cvt_pk_bf16_f32 v8, v14, v15
	v_cvt_pk_bf16_f32 v9, v12, v13
	global_store_dwordx4 v[10:11], v[6:9], off nt
	v_pk_mul_f32 v[12:13], v[100:101], s[18:19] op_sel_hi:[1,0]
	v_pk_mul_f32 v[14:15], v[98:99], s[18:19] op_sel_hi:[1,0]
	v_pk_mul_f32 v[8:9], v[104:105], s[18:19] op_sel_hi:[1,0]
	v_pk_mul_f32 v[6:7], v[102:103], s[18:19] op_sel_hi:[1,0]
	s_nop 0
	v_cvt_pk_bf16_f32 v6, v6, v7
	v_cvt_pk_bf16_f32 v7, v8, v9
	v_cvt_pk_bf16_f32 v8, v14, v15
	v_cvt_pk_bf16_f32 v9, v12, v13
	global_store_dwordx4 v[10:11], v[6:9], off offset:256 nt
	v_pk_mul_f32 v[12:13], v[92:93], s[18:19] op_sel_hi:[1,0]
	v_pk_mul_f32 v[14:15], v[90:91], s[18:19] op_sel_hi:[1,0]
	v_mad_i64_i32 v[6:7], s[44:45], v0, s65, v[2:3]
; #define LAS __attribute__((address_space(3)))
; __device__ __forceinline__ int opaque_tid() { int t = threadIdx.x; asm volatile("" : "+v"(t)); return t; }
; __device__ __forceinline__ unsigned pk2(float a, float b) { f32x2 v = {a, b}; bf16x2_t r = __builtin_convertvector(v, bf16x2_t); return __builtin_bit_cast(unsigned, r); }
;     __device__ __forceinline__ void operator()(int ui) { if (ui == slot) run(); }
;     __device__ __forceinline__ void run() { done = true;
;         const int tid_ = opaque_tid(), wave = tid_ >> 6, lane = tid_ & 63;
;         if (wave < 7) { LAS unsigned* scr = (LAS unsigned*)(lds + 131072) + wave * (64 * 17);
;             for (int v = (int)blockIdx.x * 7 + wave; v < cv::N_GW + cv::I_IN1 + cv::I_OUT; v += (int)gridDim.x * 7) conv_dispatch(*p, v < cv::N_GW ? cv::I_IN0 + cv::I_OUT + v : cv::I_L0 + (v - cv::N_GW), scr, lane); } }
;     __device__ __forceinline__ void operator()(const f32x4 (&acc)[2][2][4][2], const Unit& u, int wr, int wc, int fr, int fq) const {
;         const int row0 = u.pm * BM + wr * 64 + fr, col0 = u.pn * BM + wc * 32 + 8 * fq;
; #pragma unroll
;         for (int ai = 0; ai < 2; ++ai)
; #pragma unroll
;             for (int m = 0; m < 4; ++m) { bf16_t* rowp = O + (size_t)(row0 + ai * HALF + m * 16) * ldc + col0;
; #pragma unroll
;                 for (int bj = 0; bj < 2; ++bj) { const f32x4 v0 = acc[ai][bj][m][0] * sc, v1 = acc[ai][bj][m][1] * sc;
;                     u32x4 w; w.x = pk2(v0[0], v0[1]); w.y = pk2(v0[2], v0[3]); w.z = pk2(v1[0], v1[1]); w.w = pk2(v1[2], v1[3]);
;                     *(u32x4*)(rowp + bj * HALF) = w; } }
	v_lshl_add_u64 v[10:11], v[6:7], 0, v[4:5]
	v_pk_mul_f32 v[8:9], v[96:97], s[18:19] op_sel_hi:[1,0]
	v_pk_mul_f32 v[6:7], v[94:95], s[18:19] op_sel_hi:[1,0]
	v_add_u32_e32 v0, 0x90, v16
	v_cvt_pk_bf16_f32 v6, v6, v7
	v_cvt_pk_bf16_f32 v7, v8, v9
	v_cvt_pk_bf16_f32 v8, v14, v15
	v_cvt_pk_bf16_f32 v9, v12, v13
	global_store_dwordx4 v[10:11], v[6:9], off nt
	v_pk_mul_f32 v[12:13], v[76:77], s[18:19] op_sel_hi:[1,0]
	v_pk_mul_f32 v[14:15], v[74:75], s[18:19] op_sel_hi:[1,0]
	v_pk_mul_f32 v[8:9], v[84:85], s[18:19] op_sel_hi:[1,0]
	v_pk_mul_f32 v[6:7], v[82:83], s[18:19] op_sel_hi:[1,0]
	s_nop 0
	v_cvt_pk_bf16_f32 v6, v6, v7
	v_cvt_pk_bf16_f32 v7, v8, v9
	v_cvt_pk_bf16_f32 v8, v14, v15
	v_cvt_pk_bf16_f32 v9, v12, v13
	global_store_dwordx4 v[10:11], v[6:9], off offset:256 nt
	v_pk_mul_f32 v[12:13], v[80:81], s[18:19] op_sel_hi:[1,0]
	v_pk_mul_f32 v[14:15], v[78:79], s[18:19] op_sel_hi:[1,0]
	v_mad_i64_i32 v[6:7], s[44:45], v0, s65, v[2:3]
	v_lshl_add_u64 v[10:11], v[6:7], 0, v[4:5]
	v_pk_mul_f32 v[8:9], v[88:89], s[18:19] op_sel_hi:[1,0]
	v_pk_mul_f32 v[6:7], v[86:87], s[18:19] op_sel_hi:[1,0]
	v_add_u32_e32 v0, 0xa0, v16
	v_cvt_pk_bf16_f32 v6, v6, v7
	v_cvt_pk_bf16_f32 v7, v8, v9
	v_cvt_pk_bf16_f32 v8, v14, v15
	v_cvt_pk_bf16_f32 v9, v12, v13
	global_store_dwordx4 v[10:11], v[6:9], off nt
	v_pk_mul_f32 v[12:13], v[60:61], s[18:19] op_sel_hi:[1,0]
	v_pk_mul_f32 v[14:15], v[58:59], s[18:19] op_sel_hi:[1,0]
	v_pk_mul_f32 v[8:9], v[68:69], s[18:19] op_sel_hi:[1,0]
	v_pk_mul_f32 v[6:7], v[66:67], s[18:19] op_sel_hi:[1,0]
	s_nop 0
	v_cvt_pk_bf16_f32 v6, v6, v7
	v_cvt_pk_bf16_f32 v7, v8, v9
	v_cvt_pk_bf16_f32 v8, v14, v15
	v_cvt_pk_bf16_f32 v9, v12, v13
	global_store_dwordx4 v[10:11], v[6:9], off offset:256 nt
	v_pk_mul_f32 v[12:13], v[64:65], s[18:19] op_sel_hi:[1,0]
	v_pk_mul_f32 v[14:15], v[62:63], s[18:19] op_sel_hi:[1,0]
	v_mad_i64_i32 v[6:7], s[44:45], v0, s65, v[2:3]
	v_lshl_add_u64 v[10:11], v[6:7], 0, v[4:5]
	v_pk_mul_f32 v[8:9], v[72:73], s[18:19] op_sel_hi:[1,0]
	v_pk_mul_f32 v[6:7], v[70:71], s[18:19] op_sel_hi:[1,0]
	v_add_u32_e32 v0, 0xb0, v16
	v_cvt_pk_bf16_f32 v6, v6, v7
	v_cvt_pk_bf16_f32 v7, v8, v9
	v_cvt_pk_bf16_f32 v8, v14, v15
	v_cvt_pk_bf16_f32 v9, v12, v13
	global_store_dwordx4 v[10:11], v[6:9], off nt
	v_pk_mul_f32 v[12:13], v[44:45], s[18:19] op_sel_hi:[1,0]
	v_pk_mul_f32 v[14:15], v[42:43], s[18:19] op_sel_hi:[1,0]
	v_pk_mul_f32 v[8:9], v[52:53], s[18:19] op_sel_hi:[1,0]
	v_pk_mul_f32 v[6:7], v[50:51], s[18:19] op_sel_hi:[1,0]
	v_mad_i64_i32 v[2:3], s[44:45], v0, s65, v[2:3]
	v_cvt_pk_bf16_f32 v6, v6, v7
	v_cvt_pk_bf16_f32 v7, v8, v9
	v_cvt_pk_bf16_f32 v8, v14, v15
	v_cvt_pk_bf16_f32 v9, v12, v13
	global_store_dwordx4 v[10:11], v[6:9], off offset:256 nt
	v_pk_mul_f32 v[10:11], v[46:47], s[18:19] op_sel_hi:[1,0]
	s_nop 0
	v_lshl_add_u64 v[6:7], v[2:3], 0, v[4:5]
	v_pk_mul_f32 v[4:5], v[56:57], s[18:19] op_sel_hi:[1,0]
	v_pk_mul_f32 v[2:3], v[54:55], s[18:19] op_sel_hi:[1,0]
	v_pk_mul_f32 v[8:9], v[48:49], s[18:19] op_sel_hi:[1,0]
	v_cvt_pk_bf16_f32 v2, v2, v3
	v_cvt_pk_bf16_f32 v3, v4, v5
	v_cvt_pk_bf16_f32 v4, v10, v11
	v_cvt_pk_bf16_f32 v5, v8, v9
	global_store_dwordx4 v[6:7], v[2:5], off nt
	v_pk_mul_f32 v[8:9], v[36:37], s[18:19] op_sel_hi:[1,0]
	v_pk_mul_f32 v[10:11], v[34:35], s[18:19] op_sel_hi:[1,0]
	v_pk_mul_f32 v[4:5], v[40:41], s[18:19] op_sel_hi:[1,0]
	v_pk_mul_f32 v[2:3], v[38:39], s[18:19] op_sel_hi:[1,0]
	s_nop 0
	v_cvt_pk_bf16_f32 v2, v2, v3
	v_cvt_pk_bf16_f32 v3, v4, v5
	v_cvt_pk_bf16_f32 v4, v10, v11
	v_cvt_pk_bf16_f32 v5, v8, v9
	global_store_dwordx4 v[6:7], v[2:5], off offset:256 nt
	s_cbranch_scc1 .LBB0_169
	s_nop 0
	v_mov_b32_e32 v2, v241
	s_nop 0
	v_ashrrev_i32_e32 v3, 6, v2
	v_cmp_gt_i32_e32 vcc, 7, v3
	s_and_saveexec_b64 s[44:45], vcc
	s_cbranch_execz .LBB0_173
	s_mul_i32 s6, s2, 7
	v_add_u32_e32 v67, s6, v3
	s_movk_i32 s6, 0x1100
	v_mul_lo_u32 v0, v3, s6
	v_bfe_u32 v76, v2, 4, 2
	v_and_b32_e32 v3, 15, v2
	v_bfe_u32 v79, v2, 2, 4
	v_lshlrev_b32_e32 v2, 4, v2
	v_add_u32_e32 v0, s71, v0
	v_lshlrev_b32_e32 v66, 2, v3
	v_lshlrev_b32_e32 v4, 13, v76
	v_mul_u32_u24_e32 v3, 0x110, v3
	v_lshlrev_b32_e32 v77, 2, v76
	v_and_b32_e32 v68, 48, v2
	v_or_b32_e32 v82, 16, v79
	v_add3_u32 v78, v0, v3, v77
	v_add_u32_e32 v80, v0, v68
	v_mov_b32_e32 v69, v163
	v_mul_u32_u24_e32 v81, 0x44, v79
	v_or_b32_e32 v83, 32, v79
	v_or_b32_e32 v84, 48, v79
	v_lshl_add_u32 v85, v82, 1, v176
	s_mov_b64 s[46:47], 0
	v_lshlrev_b32_e32 v86, 2, v4
	s_branch .LBB0_157

; #define LAS __attribute__((address_space(3)))
; __device__ __forceinline__ unsigned pk4_fp8(float a, float b, float c, float d) { unsigned w = 0u; w = __builtin_amdgcn_cvt_pk_fp8_f32(a, b, w, false); w = __builtin_amdgcn_cvt_pk_fp8_f32(c, d, w, true); return w; }
; __device__ __forceinline__ void conv_item8(const float* W, int K, int N, unsigned char* WT, int k0, int n0, int drow0, LAS unsigned* scr, int lane, float sc, bool rperm = false) {
;     const int q = lane >> 4, n4 = lane & 15;
;     f32x4 v[4][4];
; #pragma unroll
;     for (int i = 0; i < 4; ++i)
; #pragma unroll
;         for (int t = 0; t < 4; ++t) v[i][t] = __builtin_nontemporal_load((const f32x4*)(W + (size_t)(k0 + 4 * (4 * i + q) + t) * N + n0 + 4 * n4));
; #pragma unroll
;     for (int i = 0; i < 4; ++i) { const int rp = 4 * i + q; LAS unsigned* sp = scr + (4 * n4) * 17 + rp;
;         sp[0]  = pk4_fp8(v[i][0].x * sc, v[i][1].x * sc, v[i][2].x * sc, v[i][3].x * sc);
;         sp[17] = pk4_fp8(v[i][0].y * sc, v[i][1].y * sc, v[i][2].y * sc, v[i][3].y * sc);
;         sp[34] = pk4_fp8(v[i][0].z * sc, v[i][1].z * sc, v[i][2].z * sc, v[i][3].z * sc);
;         sp[51] = pk4_fp8(v[i][0].w * sc, v[i][1].w * sc, v[i][2].w * sc, v[i][3].w * sc); }
; __device__ __forceinline__ void conv_dispatch(const Params& p, int it, LAS unsigned* scr, int lane) {
;     ...
;     { const int e = r / 512, rr = r % 512, kb = rr / 32, nb = rr % 32;
;         conv_item8(p.in[l ? 23 : 12] + (size_t)e * DFF * D, DFF, D, (l ? p.wp[IX_WD1] : p.wp[IX_WD0]) + (size_t)e * D * DFF, kb * 64, nb * 64, nb * 64, scr, lane, F8_SWD); }
.LBB0_157:
	s_movk_i32 s6, 0x4800
	v_cmp_gt_i32_e32 vcc, s6, v67
	s_movk_i32 s6, 0x73ff
	s_nop 0
	v_cndmask_b32_e32 v0, v177, v178, vcc
	v_add_u32_e32 v0, v0, v67
	v_add_u32_e32 v3, 0xffff8c00, v0
	v_cmp_lt_i32_e32 vcc, s6, v0
	s_nop 1
	v_cndmask_b32_e32 v2, v179, v180, vcc
	v_cndmask_b32_e32 v4, v0, v3, vcc
	v_cmp_ge_i32_e64 s[6:7], v4, v2
	s_and_saveexec_b64 s[8:9], s[6:7]
	s_xor_b64 s[8:9], exec, s[8:9]
	s_cbranch_execz .LBB0_167
	v_sub_u32_e32 v5, v4, v2
	s_movk_i32 s6, 0x3ff
	v_cmp_lt_i32_e64 s[6:7], s6, v5
	s_and_saveexec_b64 s[48:49], s[6:7]
	s_xor_b64 s[48:49], exec, s[48:49]
	s_cbranch_execz .LBB0_164
	s_movk_i32 s6, 0x43ff
	v_cmp_lt_u32_e64 s[6:7], s6, v5
	s_and_saveexec_b64 s[50:51], s[6:7]
	s_xor_b64 s[50:51], exec, s[50:51]
	s_cbranch_execz .LBB0_161
	v_cndmask_b32_e32 v162, v181, v182, vcc
	v_lshl_add_u64 v[6:7], s[0:1], 0, v[162:163]
	global_load_dwordx2 v[6:7], v[6:7], off
	v_add_u32_e32 v0, 0xffffbc00, v5
	v_lshrrev_b32_e32 v2, 9, v0
	v_mov_b32_e32 v3, v163
	v_lshlrev_b64 v[8:9], 23, v[2:3]
	v_cndmask_b32_e32 v162, v183, v184, vcc
	v_lshlrev_b32_e32 v0, 1, v4
	v_and_b32_e32 v72, 0x3c0, v0
	v_lshlrev_b32_e32 v0, 6, v4
	v_and_b32_e32 v74, 0x7c0, v0
	v_lshlrev_b64 v[2:3], 21, v[2:3]
	v_mov_b32_e32 v73, v163
	s_waitcnt vmcnt(0)
	v_lshl_add_u64 v[6:7], v[6:7], 0, v[8:9]
	v_lshl_add_u64 v[8:9], s[0:1], 0, v[162:163]
	global_load_dwordx2 v[8:9], v[8:9], off
	v_lshlrev_b32_e32 v162, 2, v74
	s_waitcnt vmcnt(0)
	v_lshl_add_u64 v[70:71], v[8:9], 0, v[2:3]
	v_lshl_add_u64 v[2:3], v[6:7], 0, v[162:163]
	v_lshlrev_b32_e32 v162, 2, v66
	v_lshl_add_u64 v[2:3], v[2:3], 0, v[162:163]
	v_lshl_or_b32 v162, v72, 13, v86
	v_lshl_add_u64 v[18:19], v[2:3], 0, v[162:163]
	v_add_co_u32_e64 v2, s[6:7], s57, v18
	global_load_dwordx4 v[50:53], v[18:19], off nt
	s_nop 0
	v_addc_co_u32_e64 v3, s[6:7], 0, v19, s[6:7]
	s_movk_i32 s6, 0x4000
	global_load_dwordx4 v[54:57], v[2:3], off nt
	v_add_co_u32_e64 v2, s[6:7], s6, v18
	s_nop 1
	v_addc_co_u32_e64 v3, s[6:7], 0, v19, s[6:7]
	s_movk_i32 s6, 0x6000
	global_load_dwordx4 v[58:61], v[2:3], off nt
	v_add_co_u32_e64 v2, s[6:7], s6, v18
	s_nop 1
	v_addc_co_u32_e64 v3, s[6:7], 0, v19, s[6:7]
	s_mov_b32 s6, 0x20000
	global_load_dwordx4 v[62:65], v[2:3], off nt
	v_add_co_u32_e64 v2, s[6:7], s6, v18
	s_nop 1
	v_addc_co_u32_e64 v3, s[6:7], 0, v19, s[6:7]
	s_mov_b32 s6, 0x22000
	global_load_dwordx4 v[34:37], v[2:3], off nt
	v_add_co_u32_e64 v2, s[6:7], s6, v18
	s_nop 1
	v_addc_co_u32_e64 v3, s[6:7], 0, v19, s[6:7]
	s_mov_b32 s6, 0x24000
	global_load_dwordx4 v[38:41], v[2:3], off nt
	v_add_co_u32_e64 v2, s[6:7], s6, v18
	s_nop 0
	s_nop 0
	v_addc_co_u32_e64 v3, s[6:7], 0, v19, s[6:7]
	s_mov_b32 s6, 0x26000
	global_load_dwordx4 v[42:45], v[2:3], off nt
	v_add_co_u32_e64 v2, s[6:7], s6, v18
	s_nop 0
	s_nop 0
	v_addc_co_u32_e64 v3, s[6:7], 0, v19, s[6:7]
	s_mov_b32 s6, 0x40000
	global_load_dwordx4 v[46:49], v[2:3], off nt
	v_add_co_u32_e64 v2, s[6:7], s6, v18
	s_nop 0
	s_nop 0
	v_addc_co_u32_e64 v3, s[6:7], 0, v19, s[6:7]
	s_mov_b32 s6, 0x42000
	s_nop 0
	v_add_co_u32_e64 v6, s[6:7], s6, v18
	global_load_dwordx4 v[2:5], v[2:3], off nt
	s_nop 0
	v_addc_co_u32_e64 v7, s[6:7], 0, v19, s[6:7]
	global_load_dwordx4 v[22:25], v[6:7], off nt
	v_add_co_u32_e64 v6, s[6:7], s72, v18
	s_nop 0
	s_nop 0
	v_addc_co_u32_e64 v7, s[6:7], 0, v19, s[6:7]
	global_load_dwordx4 v[26:29], v[6:7], off nt
	v_add_co_u32_e64 v6, s[6:7], s73, v18
	s_nop 0
	s_nop 0
	v_addc_co_u32_e64 v7, s[6:7], 0, v19, s[6:7]
	global_load_dwordx4 v[30:33], v[6:7], off nt
	v_add_co_u32_e64 v6, s[6:7], s74, v18
	s_nop 0
	s_nop 0
	v_addc_co_u32_e64 v7, s[6:7], 0, v19, s[6:7]
	v_add_co_u32_e64 v10, s[6:7], s75, v18
	global_load_dwordx4 v[6:9], v[6:7], off nt
	s_nop 0
	v_addc_co_u32_e64 v11, s[6:7], 0, v19, s[6:7]
	global_load_dwordx4 v[10:13], v[10:11], off nt
	v_add_co_u32_e64 v14, s[6:7], s76, v18
	s_nop 0
	s_nop 0
	v_addc_co_u32_e64 v15, s[6:7], 0, v19, s[6:7]
	v_add_co_u32_e64 v18, s[6:7], s77, v18
	global_load_dwordx4 v[14:17], v[14:15], off nt
	s_nop 0
	v_addc_co_u32_e64 v19, s[6:7], 0, v19, s[6:7]
	global_load_dwordx4 v[18:21], v[18:19], off nt
	s_waitcnt vmcnt(15)
	v_mul_f32_e32 v0, 0x43800000, v50
	s_waitcnt vmcnt(14)
	v_mul_f32_e32 v50, 0x43800000, v54
	s_waitcnt vmcnt(13)
	v_mul_f32_e32 v54, 0x43800000, v58
	s_waitcnt vmcnt(12)
	v_mul_f32_e32 v58, 0x43800000, v62
	v_mov_b32_e32 v62, v163
	v_cvt_pk_fp8_f32 v62, v0, v50
	v_mul_f32_e32 v0, 0x43800000, v51
	v_mul_f32_e32 v50, 0x43800000, v55
	v_mov_b32_e32 v55, v163
	v_cvt_pk_fp8_f32 v55, v0, v50
	v_cvt_pk_fp8_f32 v62, v54, v58 op_sel:[0,0,1]
	v_mul_f32_e32 v51, 0x43800000, v59
	v_mul_f32_e32 v54, 0x43800000, v63
	v_cvt_pk_fp8_f32 v55, v51, v54 op_sel:[0,0,1]
	v_mul_f32_e32 v0, 0x43800000, v52
	v_mul_f32_e32 v50, 0x43800000, v56
	v_mov_b32_e32 v54, v163
	v_cvt_pk_fp8_f32 v54, v0, v50
	v_mul_f32_e32 v0, 0x43800000, v53
	v_mul_f32_e32 v50, 0x43800000, v57
	v_mov_b32_e32 v53, v163
	v_cvt_pk_fp8_f32 v53, v0, v50
	v_mul_f32_e32 v51, 0x43800000, v60
	s_waitcnt vmcnt(11)
	v_mul_f32_e32 v0, 0x43800000, v34
	v_mul_f32_e32 v52, 0x43800000, v64
	v_cvt_pk_fp8_f32 v54, v51, v52 op_sel:[0,0,1]
	v_mul_f32_e32 v51, 0x43800000, v61
	v_mul_f32_e32 v52, 0x43800000, v65
	v_cvt_pk_fp8_f32 v53, v51, v52 op_sel:[0,0,1]
	s_waitcnt vmcnt(10)
	v_mul_f32_e32 v34, 0x43800000, v38
	s_waitcnt vmcnt(9)
	v_mul_f32_e32 v38, 0x43800000, v42
	s_waitcnt vmcnt(8)
; #define LAS __attribute__((address_space(3)))
; __device__ __forceinline__ unsigned pk4_fp8(float a, float b, float c, float d) { unsigned w = 0u; w = __builtin_amdgcn_cvt_pk_fp8_f32(a, b, w, false); w = __builtin_amdgcn_cvt_pk_fp8_f32(c, d, w, true); return w; }
; __device__ __forceinline__ void conv_item8(const float* W, int K, int N, unsigned char* WT, int k0, int n0, int drow0, LAS unsigned* scr, int lane, float sc, bool rperm = false) {
;     ...
;     for (int i = 0; i < 4; ++i) { const int rp = 4 * i + q; LAS unsigned* sp = scr + (4 * n4) * 17 + rp;
;         sp[0]  = pk4_fp8(v[i][0].x * sc, v[i][1].x * sc, v[i][2].x * sc, v[i][3].x * sc);
;         sp[17] = pk4_fp8(v[i][0].y * sc, v[i][1].y * sc, v[i][2].y * sc, v[i][3].y * sc);
;         sp[34] = pk4_fp8(v[i][0].z * sc, v[i][1].z * sc, v[i][2].z * sc, v[i][3].z * sc);
;         sp[51] = pk4_fp8(v[i][0].w * sc, v[i][1].w * sc, v[i][2].w * sc, v[i][3].w * sc); }
;     asm volatile("s_waitcnt lgkmcnt(0)" ::: "memory");
;     const int c = lane & 3;
; #pragma unroll
;     for (int j = 0; j < 4; ++j) {
;         const int n = (lane >> 2) + 16 * j; const LAS unsigned* sp = scr + n * 17 + 4 * c;
;         u32x4 o; o.x = sp[0]; o.y = sp[1]; o.z = sp[2]; o.w = sp[3];
;         const int nr = (rperm && n < 32) ? ((n < 16) ? 2 * n : 2 * (n - 16) + 1) : n;
;         *(u32x4*)(WT + (size_t)(drow0 + nr) * K + k0 + 16 * c) = o;
;     }
;     asm volatile("s_waitcnt lgkmcnt(0)" ::: "memory");
	v_mul_f32_e32 v42, 0x43800000, v46
	v_mov_b32_e32 v46, v163
	v_cvt_pk_fp8_f32 v46, v0, v34
	v_mul_f32_e32 v0, 0x43800000, v35
	v_mul_f32_e32 v34, 0x43800000, v39
	v_mov_b32_e32 v39, v163
	v_cvt_pk_fp8_f32 v39, v0, v34
	v_cvt_pk_fp8_f32 v46, v38, v42 op_sel:[0,0,1]
	v_mul_f32_e32 v35, 0x43800000, v43
	v_mul_f32_e32 v38, 0x43800000, v47
	v_cvt_pk_fp8_f32 v39, v35, v38 op_sel:[0,0,1]
	v_mul_f32_e32 v0, 0x43800000, v36
	v_mul_f32_e32 v34, 0x43800000, v40
	v_mov_b32_e32 v38, v163
	v_cvt_pk_fp8_f32 v38, v0, v34
	v_mul_f32_e32 v0, 0x43800000, v37
	v_mul_f32_e32 v34, 0x43800000, v41
	v_mov_b32_e32 v37, v163
	v_cvt_pk_fp8_f32 v37, v0, v34
	s_waitcnt vmcnt(7)
	v_mul_f32_e32 v0, 0x43800000, v2
	s_waitcnt vmcnt(6)
	v_mul_f32_e32 v2, 0x43800000, v22
	s_waitcnt vmcnt(5)
	v_mul_f32_e32 v22, 0x43800000, v26
	v_mul_f32_e32 v35, 0x43800000, v44
	v_mul_f32_e32 v36, 0x43800000, v48
	s_waitcnt vmcnt(4)
	v_mul_f32_e32 v26, 0x43800000, v30
	v_mov_b32_e32 v30, v163
	v_cvt_pk_fp8_f32 v30, v0, v2
	v_mul_f32_e32 v0, 0x43800000, v3
	v_mul_f32_e32 v2, 0x43800000, v23
	v_mov_b32_e32 v23, v163
	v_cvt_pk_fp8_f32 v23, v0, v2
	v_cvt_pk_fp8_f32 v30, v22, v26 op_sel:[0,0,1]
	v_mul_f32_e32 v3, 0x43800000, v27
	v_mul_f32_e32 v22, 0x43800000, v31
	v_cvt_pk_fp8_f32 v23, v3, v22 op_sel:[0,0,1]
	v_mul_f32_e32 v0, 0x43800000, v4
	v_mul_f32_e32 v2, 0x43800000, v24
	v_mov_b32_e32 v22, v163
	v_cvt_pk_fp8_f32 v22, v0, v2
	v_mul_f32_e32 v0, 0x43800000, v5
	v_mul_f32_e32 v2, 0x43800000, v25
	v_mov_b32_e32 v5, v163
	v_cvt_pk_fp8_f32 v5, v0, v2
	s_waitcnt vmcnt(3)
	v_mul_f32_e32 v0, 0x43800000, v6
	s_waitcnt vmcnt(2)
	v_mul_f32_e32 v2, 0x43800000, v10
	v_mov_b32_e32 v6, v163
	v_cvt_pk_fp8_f32 v6, v0, v2
	v_mul_f32_e32 v3, 0x43800000, v28
	v_mul_f32_e32 v4, 0x43800000, v32
	v_cvt_pk_fp8_f32 v22, v3, v4 op_sel:[0,0,1]
	v_mul_f32_e32 v3, 0x43800000, v29
	v_mul_f32_e32 v4, 0x43800000, v33
	v_cvt_pk_fp8_f32 v5, v3, v4 op_sel:[0,0,1]
	s_waitcnt vmcnt(1)
	v_mul_f32_e32 v3, 0x43800000, v14
	s_waitcnt vmcnt(0)
	v_mul_f32_e32 v4, 0x43800000, v18
	v_cvt_pk_fp8_f32 v6, v3, v4 op_sel:[0,0,1]
	v_mul_f32_e32 v0, 0x43800000, v7
	v_mul_f32_e32 v2, 0x43800000, v11
	v_mul_f32_e32 v3, 0x43800000, v15
	ds_write2_b32 v78, v30, v6 offset0:8 offset1:12
	v_mov_b32_e32 v6, v163
	v_cvt_pk_fp8_f32 v6, v0, v2
	v_mul_f32_e32 v4, 0x43800000, v19
	v_mul_f32_e32 v0, 0x43800000, v8
	v_mul_f32_e32 v2, 0x43800000, v12
	v_cvt_pk_fp8_f32 v6, v3, v4 op_sel:[0,0,1]
	v_mul_f32_e32 v3, 0x43800000, v16
	v_mul_f32_e32 v4, 0x43800000, v20
	v_cvt_pk_fp8_f32 v38, v35, v36 op_sel:[0,0,1]
	ds_write2_b32 v78, v23, v6 offset0:25 offset1:29
	v_mov_b32_e32 v6, v163
	v_cvt_pk_fp8_f32 v6, v0, v2
	v_mul_f32_e32 v0, 0x43800000, v9
	v_mul_f32_e32 v2, 0x43800000, v13
	v_mul_f32_e32 v35, 0x43800000, v45
	v_cvt_pk_fp8_f32 v6, v3, v4 op_sel:[0,0,1]
	v_mul_f32_e32 v36, 0x43800000, v49
	v_mul_f32_e32 v3, 0x43800000, v17
	v_mul_f32_e32 v4, 0x43800000, v21
	ds_write2_b32 v78, v22, v6 offset0:42 offset1:46
	v_mov_b32_e32 v6, v163
	v_cvt_pk_fp8_f32 v6, v0, v2
	v_cvt_pk_fp8_f32 v37, v35, v36 op_sel:[0,0,1]
	ds_write2_b32 v78, v62, v46 offset1:4
	ds_write2_b32 v78, v55, v39 offset0:17 offset1:21
	v_cvt_pk_fp8_f32 v6, v3, v4 op_sel:[0,0,1]
	ds_write2_b32 v78, v54, v38 offset0:34 offset1:38
	ds_write2_b32 v78, v53, v37 offset0:51 offset1:55
	v_lshl_add_u64 v[2:3], v[70:71], 0, v[72:73]
	ds_write2_b32 v78, v5, v6 offset0:59 offset1:63
	s_waitcnt lgkmcnt(0)
	v_add_u32_e32 v0, v80, v81
	v_lshl_add_u64 v[6:7], v[2:3], 0, v[68:69]
	ds_read2_b32 v[2:3], v0 offset1:1
	ds_read2_b32 v[4:5], v0 offset0:2 offset1:3
	v_or_b32_e32 v8, v74, v79
	v_lshlrev_b32_e32 v162, 10, v8
	v_lshl_add_u64 v[8:9], v[6:7], 0, v[162:163]
	s_waitcnt lgkmcnt(0)
	global_store_dwordx4 v[8:9], v[2:5], off nt
	v_or_b32_e32 v8, v74, v82
	s_nop 0
	v_add_u32_e32 v2, 0x440, v0
	v_add_u32_e32 v4, 0x448, v0
	ds_read2_b32 v[2:3], v2 offset1:1
	ds_read2_b32 v[4:5], v4 offset1:1
	v_lshlrev_b32_e32 v162, 10, v8
	v_lshl_add_u64 v[8:9], v[6:7], 0, v[162:163]
	s_waitcnt lgkmcnt(0)
	global_store_dwordx4 v[8:9], v[2:5], off nt
	s_nop 1
	v_add_u32_e32 v2, 0x880, v0
	v_add_u32_e32 v4, 0x888, v0
	ds_read2_b32 v[2:3], v2 offset1:1
	ds_read2_b32 v[4:5], v4 offset1:1
	v_or_b32_e32 v8, v74, v83
	v_lshlrev_b32_e32 v162, 10, v8
	v_lshl_add_u64 v[8:9], v[6:7], 0, v[162:163]
	s_waitcnt lgkmcnt(0)
	global_store_dwordx4 v[8:9], v[2:5], off nt
	s_nop 1
	v_add_u32_e32 v2, 0xcc0, v0
	v_add_u32_e32 v0, 0xcc8, v0
	ds_read2_b32 v[2:3], v2 offset1:1
	ds_read2_b32 v[4:5], v0 offset1:1
	v_or_b32_e32 v0, v74, v84
	v_lshlrev_b32_e32 v162, 10, v0
	v_lshl_add_u64 v[6:7], v[6:7], 0, v[162:163]
	s_waitcnt lgkmcnt(0)
	global_store_dwordx4 v[6:7], v[2:5], off nt
	s_waitcnt lgkmcnt(0)
; #define LAS __attribute__((address_space(3)))
; __device__ __forceinline__ unsigned pk4_fp8(float a, float b, float c, float d) { unsigned w = 0u; w = __builtin_amdgcn_cvt_pk_fp8_f32(a, b, w, false); w = __builtin_amdgcn_cvt_pk_fp8_f32(c, d, w, true); return w; }
; __device__ __forceinline__ void conv_item8(const float* W, int K, int N, unsigned char* WT, int k0, int n0, int drow0, LAS unsigned* scr, int lane, float sc, bool rperm = false) {
;     const int q = lane >> 4, n4 = lane & 15;
;     f32x4 v[4][4];
; #pragma unroll
;     for (int i = 0; i < 4; ++i)
; #pragma unroll
;         for (int t = 0; t < 4; ++t) v[i][t] = __builtin_nontemporal_load((const f32x4*)(W + (size_t)(k0 + 4 * (4 * i + q) + t) * N + n0 + 4 * n4));
; #pragma unroll
;     for (int i = 0; i < 4; ++i) { const int rp = 4 * i + q; LAS unsigned* sp = scr + (4 * n4) * 17 + rp;
;         sp[0]  = pk4_fp8(v[i][0].x * sc, v[i][1].x * sc, v[i][2].x * sc, v[i][3].x * sc);
;         sp[17] = pk4_fp8(v[i][0].y * sc, v[i][1].y * sc, v[i][2].y * sc, v[i][3].y * sc);
;         sp[34] = pk4_fp8(v[i][0].z * sc, v[i][1].z * sc, v[i][2].z * sc, v[i][3].z * sc);
;         sp[51] = pk4_fp8(v[i][0].w * sc, v[i][1].w * sc, v[i][2].w * sc, v[i][3].w * sc); }
; __device__ __forceinline__ void conv_dispatch(const Params& p, int it, LAS unsigned* scr, int lane) {
;     ...
;     if (r < 2 * I_G) { const int up = r >= I_G; if (up) r -= I_G; const int e = r / 512, rr = r % 512, kb = rr / 16, nb = rr % 16, n0 = nb * 64;
;         conv_item8(p.in[(l ? 21 : 10) + up] + (size_t)e * D * DFF, D, DFF, (l ? p.wp[IX_WGU1] : p.wp[IX_WGU0]) + (size_t)e * 2048 * D, kb * 64, n0, (n0 >> 7) * 256 + (n0 & 127) + up * 128, scr, lane, F8_SW);
.LBB0_161:
	s_andn2_saveexec_b64 s[50:51], s[50:51]
	s_cbranch_execz .LBB0_163
	v_cmp_lt_u32_e64 s[6:7], s78, v5
	v_cndmask_b32_e32 v162, v187, v188, vcc
	v_lshl_add_u64 v[6:7], s[0:1], 0, v[162:163]
	v_cndmask_b32_e64 v3, 0, 1, s[6:7]
	v_lshlrev_b32_e32 v162, 3, v3
	v_lshl_add_u64 v[6:7], v[6:7], 0, v[162:163]
	global_load_dwordx2 v[6:7], v[6:7], off
	v_cndmask_b32_e64 v0, v185, v186, s[6:7]
	v_add_u32_e32 v0, v0, v5
	v_lshrrev_b32_e32 v2, 9, v0
	v_mov_b32_e32 v3, v163
	v_lshlrev_b64 v[8:9], 23, v[2:3]
	v_cndmask_b32_e32 v162, v189, v190, vcc
	v_lshlrev_b64 v[2:3], 22, v[2:3]
	v_lshlrev_b32_e32 v5, 6, v0
	v_and_or_b32 v4, v4, s79, v76
	v_mov_b32_e32 v65, v163
	s_waitcnt vmcnt(0)
	v_lshl_add_u64 v[6:7], v[6:7], 0, v[8:9]
	v_lshl_add_u64 v[8:9], s[0:1], 0, v[162:163]
	global_load_dwordx2 v[8:9], v[8:9], off
	s_waitcnt vmcnt(0)
	v_lshl_add_u64 v[62:63], v[8:9], 0, v[2:3]
	v_lshlrev_b32_e32 v2, 2, v0
	v_and_b32_e32 v64, 0x7c0, v2
	v_lshlrev_b32_e32 v2, 7, v0
	v_lshlrev_b32_e32 v0, 8, v0
	v_and_b32_e32 v2, 0x700, v2
	v_and_b32_e32 v3, 64, v5
	v_cndmask_b32_e64 v5, 0, v191, s[6:7]
	v_and_b32_e32 v162, 0xf00, v0
	v_or3_b32 v70, v3, v5, v2
	v_lshl_add_u64 v[2:3], v[6:7], 0, v[162:163]
	v_lshlrev_b32_e32 v162, 2, v66
	v_lshl_add_u64 v[2:3], v[2:3], 0, v[162:163]
	v_lshlrev_b32_e32 v162, 14, v4
	v_lshl_add_u64 v[10:11], v[2:3], 0, v[162:163]
	v_add_co_u32_e64 v2, s[6:7], s57, v10
	global_load_dwordx4 v[50:53], v[10:11], off nt
	s_nop 0
	v_addc_co_u32_e64 v3, s[6:7], 0, v11, s[6:7]
	global_load_dwordx4 v[54:57], v[2:3], off offset:-4096 nt
	global_load_dwordx4 v[58:61], v[2:3], off nt
	s_movk_i32 s6, 0x3000
	v_add_co_u32_e64 v2, s[6:7], s6, v10
	s_nop 1
	v_addc_co_u32_e64 v3, s[6:7], 0, v11, s[6:7]
	global_load_dwordx4 v[72:75], v[2:3], off nt
	v_add_co_u32_e64 v2, s[6:7], s80, v10
	s_nop 1
	v_addc_co_u32_e64 v3, s[6:7], 0, v11, s[6:7]
	global_load_dwordx4 v[34:37], v[2:3], off offset:-4096 nt
	global_load_dwordx4 v[38:41], v[2:3], off nt
	v_add_co_u32_e64 v2, s[6:7], s81, v10
	s_nop 0
	s_nop 0
	v_addc_co_u32_e64 v3, s[6:7], 0, v11, s[6:7]
	global_load_dwordx4 v[42:45], v[2:3], off offset:-4096 nt
	global_load_dwordx4 v[46:49], v[2:3], off nt
	v_add_co_u32_e64 v2, s[6:7], s82, v10
	s_nop 0
	s_nop 0
	v_addc_co_u32_e64 v3, s[6:7], 0, v11, s[6:7]
	global_load_dwordx4 v[18:21], v[2:3], off offset:-4096 nt
	global_load_dwordx4 v[22:25], v[2:3], off nt
	v_add_co_u32_e64 v2, s[6:7], s83, v10
	s_nop 0
	s_nop 0
	v_addc_co_u32_e64 v3, s[6:7], 0, v11, s[6:7]
	global_load_dwordx4 v[26:29], v[2:3], off offset:-4096 nt
	global_load_dwordx4 v[30:33], v[2:3], off nt
	v_add_co_u32_e64 v6, s[6:7], s84, v10
	s_nop 0
	s_nop 0
	v_addc_co_u32_e64 v7, s[6:7], 0, v11, s[6:7]
	v_add_co_u32_e64 v14, s[6:7], s85, v10
	global_load_dwordx4 v[2:5], v[6:7], off offset:-4096 nt
	s_nop 0
	global_load_dwordx4 v[6:9], v[6:7], off nt
	v_addc_co_u32_e64 v15, s[6:7], 0, v11, s[6:7]
	global_load_dwordx4 v[10:13], v[14:15], off offset:-4096 nt
	s_nop 0
	global_load_dwordx4 v[14:17], v[14:15], off nt
	s_waitcnt vmcnt(15)
	v_mul_f32_e32 v0, 0x43800000, v50
	s_waitcnt vmcnt(14)
	v_mul_f32_e32 v50, 0x43800000, v54
	v_cvt_pk_fp8_f32 v65, v0, v50
	v_mul_f32_e32 v0, 0x43800000, v51
	v_mul_f32_e32 v50, 0x43800000, v55
	v_mov_b32_e32 v55, v163
	v_cvt_pk_fp8_f32 v55, v0, v50
	s_waitcnt vmcnt(13)
	v_mul_f32_e32 v54, 0x43800000, v58
	v_mul_f32_e32 v51, 0x43800000, v59
	v_mul_f32_e32 v0, 0x43800000, v52
	v_mul_f32_e32 v50, 0x43800000, v56
	s_waitcnt vmcnt(12)
	v_mul_f32_e32 v58, 0x43800000, v72
	v_cvt_pk_fp8_f32 v65, v54, v58 op_sel:[0,0,1]
	v_mul_f32_e32 v54, 0x43800000, v73
	v_cvt_pk_fp8_f32 v55, v51, v54 op_sel:[0,0,1]
	v_mov_b32_e32 v54, v163
	v_cvt_pk_fp8_f32 v54, v0, v50
	v_mul_f32_e32 v0, 0x43800000, v53
	v_mul_f32_e32 v50, 0x43800000, v57
	v_mov_b32_e32 v53, v163
	v_cvt_pk_fp8_f32 v53, v0, v50
	s_waitcnt vmcnt(11)
	v_mul_f32_e32 v0, 0x43800000, v34
	s_waitcnt vmcnt(10)
	v_mul_f32_e32 v34, 0x43800000, v38
	s_waitcnt vmcnt(9)
	v_mul_f32_e32 v38, 0x43800000, v42
	s_waitcnt vmcnt(8)
	v_mul_f32_e32 v42, 0x43800000, v46
	v_mov_b32_e32 v46, v163
	v_cvt_pk_fp8_f32 v46, v0, v34
	v_mul_f32_e32 v0, 0x43800000, v35
	v_mul_f32_e32 v34, 0x43800000, v39
	v_mov_b32_e32 v39, v163
	v_cvt_pk_fp8_f32 v39, v0, v34
	v_cvt_pk_fp8_f32 v46, v38, v42 op_sel:[0,0,1]
	v_mul_f32_e32 v35, 0x43800000, v43
	v_mul_f32_e32 v38, 0x43800000, v47
	v_cvt_pk_fp8_f32 v39, v35, v38 op_sel:[0,0,1]
	v_mul_f32_e32 v0, 0x43800000, v36
	v_mul_f32_e32 v34, 0x43800000, v40
	v_mov_b32_e32 v38, v163
	v_cvt_pk_fp8_f32 v38, v0, v34
	v_mul_f32_e32 v0, 0x43800000, v37
	v_mul_f32_e32 v34, 0x43800000, v41
	v_mov_b32_e32 v37, v163
	v_cvt_pk_fp8_f32 v37, v0, v34
	s_waitcnt vmcnt(7)
; #define LAS __attribute__((address_space(3)))
; __device__ __forceinline__ unsigned pk4_fp8(float a, float b, float c, float d) { unsigned w = 0u; w = __builtin_amdgcn_cvt_pk_fp8_f32(a, b, w, false); w = __builtin_amdgcn_cvt_pk_fp8_f32(c, d, w, true); return w; }
; __device__ __forceinline__ void conv_item8(const float* W, int K, int N, unsigned char* WT, int k0, int n0, int drow0, LAS unsigned* scr, int lane, float sc, bool rperm = false) {
;     ...
;     for (int i = 0; i < 4; ++i) { const int rp = 4 * i + q; LAS unsigned* sp = scr + (4 * n4) * 17 + rp;
;         sp[0]  = pk4_fp8(v[i][0].x * sc, v[i][1].x * sc, v[i][2].x * sc, v[i][3].x * sc);
;         sp[17] = pk4_fp8(v[i][0].y * sc, v[i][1].y * sc, v[i][2].y * sc, v[i][3].y * sc);
;         sp[34] = pk4_fp8(v[i][0].z * sc, v[i][1].z * sc, v[i][2].z * sc, v[i][3].z * sc);
;         sp[51] = pk4_fp8(v[i][0].w * sc, v[i][1].w * sc, v[i][2].w * sc, v[i][3].w * sc); }
;     asm volatile("s_waitcnt lgkmcnt(0)" ::: "memory");
;     const int c = lane & 3;
; #pragma unroll
;     for (int j = 0; j < 4; ++j) {
;         const int n = (lane >> 2) + 16 * j; const LAS unsigned* sp = scr + n * 17 + 4 * c;
;         u32x4 o; o.x = sp[0]; o.y = sp[1]; o.z = sp[2]; o.w = sp[3];
;         const int nr = (rperm && n < 32) ? ((n < 16) ? 2 * n : 2 * (n - 16) + 1) : n;
;         *(u32x4*)(WT + (size_t)(drow0 + nr) * K + k0 + 16 * c) = o;
;     }
;     asm volatile("s_waitcnt lgkmcnt(0)" ::: "memory");
	v_mul_f32_e32 v0, 0x43800000, v18
	s_waitcnt vmcnt(6)
	v_mul_f32_e32 v18, 0x43800000, v22
	s_waitcnt vmcnt(5)
	v_mul_f32_e32 v22, 0x43800000, v26
	s_waitcnt vmcnt(4)
	v_mul_f32_e32 v26, 0x43800000, v30
	v_mov_b32_e32 v30, v163
	v_cvt_pk_fp8_f32 v30, v0, v18
	v_mul_f32_e32 v0, 0x43800000, v19
	v_mul_f32_e32 v19, 0x43800000, v23
	v_mov_b32_e32 v18, v163
	v_cvt_pk_fp8_f32 v18, v0, v19
	v_cvt_pk_fp8_f32 v30, v22, v26 op_sel:[0,0,1]
	v_mul_f32_e32 v22, 0x43800000, v27
	v_mul_f32_e32 v23, 0x43800000, v31
	v_cvt_pk_fp8_f32 v18, v22, v23 op_sel:[0,0,1]
	v_mul_f32_e32 v0, 0x43800000, v20
	v_mul_f32_e32 v19, 0x43800000, v24
	v_mov_b32_e32 v23, v163
	v_cvt_pk_fp8_f32 v23, v0, v19
	v_mul_f32_e32 v20, 0x43800000, v28
	v_mul_f32_e32 v22, 0x43800000, v32
	v_mul_f32_e32 v0, 0x43800000, v21
	v_cvt_pk_fp8_f32 v23, v20, v22 op_sel:[0,0,1]
	v_mul_f32_e32 v20, 0x43800000, v25
	v_mov_b32_e32 v19, v163
	v_cvt_pk_fp8_f32 v19, v0, v20
	s_waitcnt vmcnt(3)
	v_mul_f32_e32 v0, 0x43800000, v2
	s_waitcnt vmcnt(2)
	v_mul_f32_e32 v2, 0x43800000, v6
	s_waitcnt vmcnt(1)
	v_mul_f32_e32 v6, 0x43800000, v10
	s_waitcnt vmcnt(0)
	v_mul_f32_e32 v10, 0x43800000, v14
	v_mov_b32_e32 v14, v163
	v_cvt_pk_fp8_f32 v14, v0, v2
	v_mul_f32_e32 v0, 0x43800000, v3
	v_mul_f32_e32 v2, 0x43800000, v7
	v_mov_b32_e32 v7, v163
	v_cvt_pk_fp8_f32 v7, v0, v2
	v_cvt_pk_fp8_f32 v14, v6, v10 op_sel:[0,0,1]
	v_mul_f32_e32 v3, 0x43800000, v11
	v_mul_f32_e32 v6, 0x43800000, v15
	v_cvt_pk_fp8_f32 v7, v3, v6 op_sel:[0,0,1]
	v_mul_f32_e32 v0, 0x43800000, v4
	v_mul_f32_e32 v2, 0x43800000, v8
	v_mov_b32_e32 v6, v163
	v_cvt_pk_fp8_f32 v6, v0, v2
	v_mul_f32_e32 v0, 0x43800000, v5
	v_mul_f32_e32 v2, 0x43800000, v9
	v_mov_b32_e32 v5, v163
	v_cvt_pk_fp8_f32 v5, v0, v2
	v_mul_f32_e32 v51, 0x43800000, v60
	v_mul_f32_e32 v52, 0x43800000, v74
	v_mul_f32_e32 v35, 0x43800000, v44
	v_mul_f32_e32 v36, 0x43800000, v48
	v_mul_f32_e32 v3, 0x43800000, v12
	v_mul_f32_e32 v4, 0x43800000, v16
	v_cvt_pk_fp8_f32 v54, v51, v52 op_sel:[0,0,1]
	v_mul_f32_e32 v51, 0x43800000, v61
	v_mul_f32_e32 v52, 0x43800000, v75
	v_cvt_pk_fp8_f32 v38, v35, v36 op_sel:[0,0,1]
	v_mul_f32_e32 v35, 0x43800000, v45
	v_mul_f32_e32 v36, 0x43800000, v49
	v_mul_f32_e32 v21, 0x43800000, v29
	v_mul_f32_e32 v22, 0x43800000, v33
	v_cvt_pk_fp8_f32 v6, v3, v4 op_sel:[0,0,1]
	v_mul_f32_e32 v3, 0x43800000, v13
	v_mul_f32_e32 v4, 0x43800000, v17
	v_cvt_pk_fp8_f32 v53, v51, v52 op_sel:[0,0,1]
	v_cvt_pk_fp8_f32 v37, v35, v36 op_sel:[0,0,1]
	v_cvt_pk_fp8_f32 v19, v21, v22 op_sel:[0,0,1]
	v_cvt_pk_fp8_f32 v5, v3, v4 op_sel:[0,0,1]
	ds_write2_b32 v78, v65, v46 offset1:4
	ds_write2_b32 v78, v55, v39 offset0:17 offset1:21
	ds_write2_b32 v78, v54, v38 offset0:34 offset1:38
	ds_write2_b32 v78, v53, v37 offset0:51 offset1:55
	ds_write2_b32 v78, v30, v14 offset0:8 offset1:12
	ds_write2_b32 v78, v18, v7 offset0:25 offset1:29
	ds_write2_b32 v78, v23, v6 offset0:42 offset1:46
	ds_write2_b32 v78, v19, v5 offset0:59 offset1:63
	v_mov_b32_e32 v65, v163
	s_waitcnt lgkmcnt(0)
	v_lshl_add_u64 v[2:3], v[62:63], 0, v[64:65]
	v_add_u32_e32 v0, v80, v81
	v_lshl_add_u64 v[6:7], v[2:3], 0, v[68:69]
	ds_read2_b32 v[2:3], v0 offset1:1
	ds_read2_b32 v[4:5], v0 offset0:2 offset1:3
	v_or_b32_e32 v8, v70, v79
	v_lshlrev_b32_e32 v162, 11, v8
	v_lshl_add_u64 v[8:9], v[6:7], 0, v[162:163]
	s_waitcnt lgkmcnt(0)
	global_store_dwordx4 v[8:9], v[2:5], off nt
	v_or_b32_e32 v8, v70, v82
	s_nop 0
	v_add_u32_e32 v2, 0x440, v0
	v_add_u32_e32 v4, 0x448, v0
	ds_read2_b32 v[2:3], v2 offset1:1
	ds_read2_b32 v[4:5], v4 offset1:1
	v_lshlrev_b32_e32 v162, 11, v8
	v_lshl_add_u64 v[8:9], v[6:7], 0, v[162:163]
	s_waitcnt lgkmcnt(0)
	global_store_dwordx4 v[8:9], v[2:5], off nt
	s_nop 1
	v_add_u32_e32 v2, 0x880, v0
	v_add_u32_e32 v4, 0x888, v0
	ds_read2_b32 v[2:3], v2 offset1:1
	ds_read2_b32 v[4:5], v4 offset1:1
	v_or_b32_e32 v8, v70, v83
	v_lshlrev_b32_e32 v162, 11, v8
	v_lshl_add_u64 v[8:9], v[6:7], 0, v[162:163]
	s_waitcnt lgkmcnt(0)
	global_store_dwordx4 v[8:9], v[2:5], off nt
	s_nop 1
	v_add_u32_e32 v2, 0xcc0, v0
	v_add_u32_e32 v0, 0xcc8, v0
	ds_read2_b32 v[2:3], v2 offset1:1
	ds_read2_b32 v[4:5], v0 offset1:1
	v_or_b32_e32 v0, v70, v84
	v_lshlrev_b32_e32 v162, 11, v0
	v_lshl_add_u64 v[6:7], v[6:7], 0, v[162:163]
	s_waitcnt lgkmcnt(0)
	global_store_dwordx4 v[6:7], v[2:5], off nt
	s_waitcnt lgkmcnt(0)

; #define LAS __attribute__((address_space(3)))
; __device__ __forceinline__ unsigned pk4_fp8(float a, float b, float c, float d) { unsigned w = 0u; w = __builtin_amdgcn_cvt_pk_fp8_f32(a, b, w, false); w = __builtin_amdgcn_cvt_pk_fp8_f32(c, d, w, true); return w; }
; __device__ __forceinline__ void conv_item8(const float* W, int K, int N, unsigned char* WT, int k0, int n0, int drow0, LAS unsigned* scr, int lane, float sc, bool rperm = false) {
;     const int q = lane >> 4, n4 = lane & 15;
;     f32x4 v[4][4];
; #pragma unroll
;     for (int i = 0; i < 4; ++i)
; #pragma unroll
;         for (int t = 0; t < 4; ++t) v[i][t] = __builtin_nontemporal_load((const f32x4*)(W + (size_t)(k0 + 4 * (4 * i + q) + t) * N + n0 + 4 * n4));
; #pragma unroll
;     for (int i = 0; i < 4; ++i) { const int rp = 4 * i + q; LAS unsigned* sp = scr + (4 * n4) * 17 + rp;
;         sp[0]  = pk4_fp8(v[i][0].x * sc, v[i][1].x * sc, v[i][2].x * sc, v[i][3].x * sc);
;         sp[17] = pk4_fp8(v[i][0].y * sc, v[i][1].y * sc, v[i][2].y * sc, v[i][3].y * sc);
;         sp[34] = pk4_fp8(v[i][0].z * sc, v[i][1].z * sc, v[i][2].z * sc, v[i][3].z * sc);
;         sp[51] = pk4_fp8(v[i][0].w * sc, v[i][1].w * sc, v[i][2].w * sc, v[i][3].w * sc); }
; __device__ __forceinline__ void conv_dispatch(const Params& p, int it, LAS unsigned* scr, int lane) {
;     ...
;     if (r < I_OUT) { if (OUT_F8) conv_item8(p.in[l ? 19 : 8], D, D, l ? p.wp[IX_WOUT1] : p.wp[IX_WOUT0], (r / 32) * 64, (r % 32) * 64, (r % 32) * 64, scr, lane, F8_SWD);
.LBB0_164:
	s_andn2_saveexec_b64 s[6:7], s[48:49]
	s_cbranch_execz .LBB0_166
	v_cndmask_b32_e32 v162, 64, v192, vcc
	v_lshl_add_u64 v[2:3], s[0:1], 0, v[162:163]
	global_load_dwordx2 v[2:3], v[2:3], off
	v_ashrrev_i16_e32 v0, 15, v5
	v_lshrrev_b16_e32 v0, 11, v0
	v_add_u16_e32 v0, v5, v0
	v_ashrrev_i16_e32 v4, 5, v0
	v_and_b32_e32 v0, 0xffffffe0, v0
	v_cndmask_b32_e32 v162, v193, v194, vcc
	v_lshlrev_b32_sdwa v74, v195, sext(v4) dst_sel:DWORD dst_unused:UNUSED_PAD src0_sel:DWORD src1_sel:WORD_0
	v_sub_u16_e32 v0, v5, v0
	v_lshl_add_u64 v[6:7], s[0:1], 0, v[162:163]
	v_lshlrev_b32_sdwa v70, v195, sext(v0) dst_sel:DWORD dst_unused:UNUSED_PAD src0_sel:DWORD src1_sel:WORD_0
	v_or_b32_e32 v50, v74, v77
	global_load_dwordx2 v[72:73], v[6:7], off
	v_ashrrev_i32_e32 v71, 31, v70
	v_or_b32_e32 v4, 1, v50
	v_or_b32_e32 v6, 2, v50
	v_or_b32_e32 v8, 3, v50
	v_lshlrev_b32_e32 v162, 2, v66
	v_ashrrev_i32_e32 v51, 31, v50
	v_ashrrev_i32_e32 v5, 31, v4
	v_ashrrev_i32_e32 v7, 31, v6
	v_ashrrev_i32_e32 v9, 31, v8
	v_or_b32_e32 v10, 16, v50
	v_or_b32_e32 v12, 17, v50
	v_or_b32_e32 v14, 18, v50
	v_or_b32_e32 v16, 19, v50
	v_lshlrev_b64 v[18:19], 13, v[50:51]
	v_lshlrev_b64 v[4:5], 13, v[4:5]
	v_lshlrev_b64 v[6:7], 13, v[6:7]
	v_lshlrev_b64 v[8:9], 13, v[8:9]
	v_ashrrev_i32_e32 v11, 31, v10
	v_ashrrev_i32_e32 v13, 31, v12
	v_ashrrev_i32_e32 v15, 31, v14
	v_ashrrev_i32_e32 v17, 31, v16
	v_or_b32_e32 v54, 32, v50
	v_or_b32_e32 v56, 33, v50
	v_or_b32_e32 v58, 34, v50
	v_or_b32_e32 v60, 35, v50
	v_ashrrev_i32_e32 v55, 31, v54
	v_ashrrev_i32_e32 v57, 31, v56
	v_ashrrev_i32_e32 v59, 31, v58
	v_ashrrev_i32_e32 v61, 31, v60
	v_mov_b32_e32 v92, v163
	v_mov_b32_e32 v96, v163
	v_mov_b32_e32 v0, v163
	v_mov_b32_e32 v93, v163
	v_mov_b32_e32 v97, v163
	v_mov_b32_e32 v75, v163
	v_mov_b32_e32 v94, v163
	v_mov_b32_e32 v87, v163
	v_mov_b32_e32 v95, v163
	s_waitcnt vmcnt(0)
	v_lshl_add_u64 v[2:3], v[70:71], 2, v[2:3]
	v_lshl_add_u64 v[52:53], v[2:3], 0, v[162:163]
	v_lshl_add_u64 v[2:3], v[52:53], 0, v[18:19]
	v_lshl_add_u64 v[4:5], v[52:53], 0, v[4:5]
	v_lshl_add_u64 v[6:7], v[52:53], 0, v[6:7]
	v_lshl_add_u64 v[8:9], v[52:53], 0, v[8:9]
	global_load_dwordx4 v[18:21], v[2:3], off nt
	global_load_dwordx4 v[22:25], v[4:5], off nt
	global_load_dwordx4 v[26:29], v[6:7], off nt
	global_load_dwordx4 v[30:33], v[8:9], off nt
	v_lshlrev_b64 v[2:3], 13, v[10:11]
	v_lshlrev_b64 v[4:5], 13, v[12:13]
	v_lshlrev_b64 v[6:7], 13, v[14:15]
	v_lshlrev_b64 v[8:9], 13, v[16:17]
	v_lshl_add_u64 v[2:3], v[52:53], 0, v[2:3]
	v_lshl_add_u64 v[4:5], v[52:53], 0, v[4:5]
	v_lshl_add_u64 v[6:7], v[52:53], 0, v[6:7]
	v_lshl_add_u64 v[8:9], v[52:53], 0, v[8:9]
	global_load_dwordx4 v[34:37], v[2:3], off nt
	global_load_dwordx4 v[38:41], v[4:5], off nt
	global_load_dwordx4 v[42:45], v[6:7], off nt
	global_load_dwordx4 v[46:49], v[8:9], off nt
	v_lshlrev_b64 v[2:3], 13, v[54:55]
	v_lshlrev_b64 v[4:5], 13, v[56:57]
	v_lshlrev_b64 v[6:7], 13, v[58:59]
	v_lshlrev_b64 v[8:9], 13, v[60:61]
	v_lshl_add_u64 v[2:3], v[52:53], 0, v[2:3]
	v_lshl_add_u64 v[4:5], v[52:53], 0, v[4:5]
	v_lshl_add_u64 v[6:7], v[52:53], 0, v[6:7]
	v_lshl_add_u64 v[8:9], v[52:53], 0, v[8:9]
	global_load_dwordx4 v[10:13], v[2:3], off nt
	global_load_dwordx4 v[14:17], v[4:5], off nt
	s_nop 0
	global_load_dwordx4 v[2:5], v[6:7], off nt
	s_nop 0
	global_load_dwordx4 v[6:9], v[8:9], off nt
	v_or_b32_e32 v54, 48, v50
	v_or_b32_e32 v56, 49, v50
	v_or_b32_e32 v58, 50, v50
	v_or_b32_e32 v50, 51, v50
	v_ashrrev_i32_e32 v55, 31, v54
	v_ashrrev_i32_e32 v57, 31, v56
	v_ashrrev_i32_e32 v59, 31, v58
	v_ashrrev_i32_e32 v51, 31, v50
	v_lshlrev_b64 v[54:55], 13, v[54:55]
	v_lshlrev_b64 v[56:57], 13, v[56:57]
	v_lshlrev_b64 v[58:59], 13, v[58:59]
	v_lshlrev_b64 v[50:51], 13, v[50:51]
	v_lshl_add_u64 v[54:55], v[52:53], 0, v[54:55]
	v_lshl_add_u64 v[56:57], v[52:53], 0, v[56:57]
	v_lshl_add_u64 v[88:89], v[52:53], 0, v[58:59]
	v_lshl_add_u64 v[90:91], v[52:53], 0, v[50:51]
	global_load_dwordx4 v[58:61], v[54:55], off nt
	global_load_dwordx4 v[62:65], v[56:57], off nt
	global_load_dwordx4 v[50:53], v[88:89], off nt
	s_nop 0
	global_load_dwordx4 v[54:57], v[90:91], off nt
	v_mov_b32_e32 v71, v163
	s_waitcnt vmcnt(15)
	v_mul_f32_e32 v18, 0x43800000, v18
	s_waitcnt vmcnt(14)
	v_mul_f32_e32 v22, 0x43800000, v22
	v_mul_f32_e32 v19, 0x43800000, v19
	v_mul_f32_e32 v23, 0x43800000, v23
	v_cvt_pk_fp8_f32 v71, v18, v22
	v_mul_f32_e32 v20, 0x43800000, v20
	v_mul_f32_e32 v24, 0x43800000, v24
	v_cvt_pk_fp8_f32 v0, v19, v23
	v_mul_f32_e32 v21, 0x43800000, v21
	s_waitcnt vmcnt(11)
	v_mul_f32_e32 v34, 0x43800000, v34
	s_waitcnt vmcnt(10)
	v_mul_f32_e32 v38, 0x43800000, v38
	v_mul_f32_e32 v35, 0x43800000, v35
	v_mul_f32_e32 v39, 0x43800000, v39
	v_cvt_pk_fp8_f32 v92, v34, v38
	v_mul_f32_e32 v36, 0x43800000, v36
	v_mul_f32_e32 v40, 0x43800000, v40
	v_cvt_pk_fp8_f32 v93, v35, v39
	v_mul_f32_e32 v25, 0x43800000, v25
	s_waitcnt vmcnt(7)
	v_mul_f32_e32 v10, 0x43800000, v10
	s_waitcnt vmcnt(6)
; #define LAS __attribute__((address_space(3)))
; __device__ __forceinline__ unsigned pk4_fp8(float a, float b, float c, float d) { unsigned w = 0u; w = __builtin_amdgcn_cvt_pk_fp8_f32(a, b, w, false); w = __builtin_amdgcn_cvt_pk_fp8_f32(c, d, w, true); return w; }
; __device__ __forceinline__ void conv_item8(const float* W, int K, int N, unsigned char* WT, int k0, int n0, int drow0, LAS unsigned* scr, int lane, float sc, bool rperm = false) {
;     ...
;     for (int i = 0; i < 4; ++i) { const int rp = 4 * i + q; LAS unsigned* sp = scr + (4 * n4) * 17 + rp;
;         sp[0]  = pk4_fp8(v[i][0].x * sc, v[i][1].x * sc, v[i][2].x * sc, v[i][3].x * sc);
;         sp[17] = pk4_fp8(v[i][0].y * sc, v[i][1].y * sc, v[i][2].y * sc, v[i][3].y * sc);
;         sp[34] = pk4_fp8(v[i][0].z * sc, v[i][1].z * sc, v[i][2].z * sc, v[i][3].z * sc);
;         sp[51] = pk4_fp8(v[i][0].w * sc, v[i][1].w * sc, v[i][2].w * sc, v[i][3].w * sc); }
;     asm volatile("s_waitcnt lgkmcnt(0)" ::: "memory");
;     const int c = lane & 3;
; #pragma unroll
;     for (int j = 0; j < 4; ++j) {
;         const int n = (lane >> 2) + 16 * j; const LAS unsigned* sp = scr + n * 17 + 4 * c;
;         u32x4 o; o.x = sp[0]; o.y = sp[1]; o.z = sp[2]; o.w = sp[3];
;         const int nr = (rperm && n < 32) ? ((n < 16) ? 2 * n : 2 * (n - 16) + 1) : n;
;         *(u32x4*)(WT + (size_t)(drow0 + nr) * K + k0 + 16 * c) = o;
;     }
;     asm volatile("s_waitcnt lgkmcnt(0)" ::: "memory");
	v_mul_f32_e32 v14, 0x43800000, v14
	v_mul_f32_e32 v11, 0x43800000, v11
	v_mul_f32_e32 v15, 0x43800000, v15
	v_cvt_pk_fp8_f32 v96, v10, v14
	v_cvt_pk_fp8_f32 v97, v11, v15
	v_mul_f32_e32 v37, 0x43800000, v37
	v_mul_f32_e32 v41, 0x43800000, v41
	v_cvt_pk_fp8_f32 v75, v20, v24
	v_cvt_pk_fp8_f32 v94, v36, v40
	v_mul_f32_e32 v26, 0x43800000, v26
	v_mul_f32_e32 v30, 0x43800000, v30
	v_mul_f32_e32 v42, 0x43800000, v42
	v_mul_f32_e32 v46, 0x43800000, v46
	s_waitcnt vmcnt(5)
	v_mul_f32_e32 v2, 0x43800000, v2
	s_waitcnt vmcnt(4)
	v_mul_f32_e32 v6, 0x43800000, v6
	v_cvt_pk_fp8_f32 v87, v21, v25
	v_cvt_pk_fp8_f32 v95, v37, v41
	v_mul_f32_e32 v27, 0x43800000, v27
	v_mul_f32_e32 v31, 0x43800000, v31
	v_mul_f32_e32 v43, 0x43800000, v43
	v_mul_f32_e32 v47, 0x43800000, v47
	v_mul_f32_e32 v3, 0x43800000, v3
	v_mul_f32_e32 v7, 0x43800000, v7
	v_mul_f32_e32 v12, 0x43800000, v12
	v_mul_f32_e32 v16, 0x43800000, v16
	v_cvt_pk_fp8_f32 v71, v26, v30 op_sel:[0,0,1]
	v_cvt_pk_fp8_f32 v92, v42, v46 op_sel:[0,0,1]
	v_cvt_pk_fp8_f32 v96, v2, v6 op_sel:[0,0,1]
	v_mov_b32_e32 v2, v163
	v_mul_f32_e32 v28, 0x43800000, v28
	v_mul_f32_e32 v32, 0x43800000, v32
	v_mul_f32_e32 v44, 0x43800000, v44
	v_mul_f32_e32 v48, 0x43800000, v48
	v_cvt_pk_fp8_f32 v0, v27, v31 op_sel:[0,0,1]
	v_cvt_pk_fp8_f32 v93, v43, v47 op_sel:[0,0,1]
	v_cvt_pk_fp8_f32 v97, v3, v7 op_sel:[0,0,1]
	v_cvt_pk_fp8_f32 v2, v12, v16
	v_mul_f32_e32 v3, 0x43800000, v13
	v_mul_f32_e32 v6, 0x43800000, v17
	v_mov_b32_e32 v7, v163
	v_mul_f32_e32 v29, 0x43800000, v29
	v_mul_f32_e32 v33, 0x43800000, v33
	v_mul_f32_e32 v45, 0x43800000, v45
	v_mul_f32_e32 v49, 0x43800000, v49
	v_cvt_pk_fp8_f32 v75, v28, v32 op_sel:[0,0,1]
	v_cvt_pk_fp8_f32 v94, v44, v48 op_sel:[0,0,1]
	v_cvt_pk_fp8_f32 v7, v3, v6
	v_cvt_pk_fp8_f32 v87, v29, v33 op_sel:[0,0,1]
	v_cvt_pk_fp8_f32 v95, v45, v49 op_sel:[0,0,1]
	v_mul_f32_e32 v4, 0x43800000, v4
	ds_write2_b32 v78, v71, v92 offset1:4
	ds_write2_b32 v78, v0, v93 offset0:17 offset1:21
	ds_write2_b32 v78, v75, v94 offset0:34 offset1:38
	ds_write2_b32 v78, v87, v95 offset0:51 offset1:55
	v_mul_f32_e32 v0, 0x43800000, v8
	v_cvt_pk_fp8_f32 v2, v4, v0 op_sel:[0,0,1]
	v_mul_f32_e32 v0, 0x43800000, v5
	v_mul_f32_e32 v3, 0x43800000, v9
	v_cvt_pk_fp8_f32 v7, v0, v3 op_sel:[0,0,1]
	s_waitcnt vmcnt(3)
	v_mul_f32_e32 v0, 0x43800000, v58
	s_waitcnt vmcnt(2)
	v_mul_f32_e32 v3, 0x43800000, v62
	v_mov_b32_e32 v6, v163
	v_cvt_pk_fp8_f32 v6, v0, v3
	v_mul_f32_e32 v0, 0x43800000, v59
	v_mul_f32_e32 v3, 0x43800000, v63
	v_mov_b32_e32 v8, v163
	v_cvt_pk_fp8_f32 v8, v0, v3
	s_waitcnt vmcnt(1)
	v_mul_f32_e32 v0, 0x43800000, v51
	s_waitcnt vmcnt(0)
	v_mul_f32_e32 v3, 0x43800000, v55
	v_mov_b32_e32 v9, v163
	v_cvt_pk_fp8_f32 v8, v0, v3 op_sel:[0,0,1]
	v_mul_f32_e32 v0, 0x43800000, v60
	v_mul_f32_e32 v3, 0x43800000, v64
	v_cvt_pk_fp8_f32 v9, v0, v3
	v_mul_f32_e32 v0, 0x43800000, v61
	v_mul_f32_e32 v3, 0x43800000, v65
	v_mov_b32_e32 v10, v163
	v_mul_f32_e32 v4, 0x43800000, v50
	v_mul_f32_e32 v5, 0x43800000, v54
	v_cvt_pk_fp8_f32 v10, v0, v3
	v_cvt_pk_fp8_f32 v6, v4, v5 op_sel:[0,0,1]
	v_mul_f32_e32 v4, 0x43800000, v52
	v_mul_f32_e32 v5, 0x43800000, v56
	v_cvt_pk_fp8_f32 v9, v4, v5 op_sel:[0,0,1]
	v_mul_f32_e32 v0, 0x43800000, v53
	v_mul_f32_e32 v3, 0x43800000, v57
	v_cvt_pk_fp8_f32 v10, v0, v3 op_sel:[0,0,1]
	ds_write2_b32 v78, v96, v6 offset0:8 offset1:12
	ds_write2_b32 v78, v97, v8 offset0:25 offset1:29
	ds_write2_b32 v78, v2, v9 offset0:42 offset1:46
	ds_write2_b32 v78, v7, v10 offset0:59 offset1:63
	v_ashrrev_i32_e32 v75, 31, v74
	s_waitcnt lgkmcnt(0)
	v_lshl_add_u64 v[2:3], v[72:73], 0, v[74:75]
	v_add_u32_e32 v0, v80, v81
	v_lshl_add_u64 v[10:11], v[2:3], 0, v[68:69]
	ds_read2_b32 v[2:3], v0 offset1:1
	ds_read2_b32 v[4:5], v0 offset0:2 offset1:3
	v_or_b32_e32 v6, v70, v79
	v_ashrrev_i32_e32 v7, 31, v6
	v_lshlrev_b64 v[6:7], 11, v[6:7]
	v_lshl_add_u64 v[12:13], v[10:11], 0, v[6:7]
	v_add_u32_e32 v6, 0x440, v0
	v_add_u32_e32 v8, 0x448, v0
	ds_read2_b32 v[6:7], v6 offset1:1
	ds_read2_b32 v[8:9], v8 offset1:1
	s_waitcnt lgkmcnt(2)
	global_store_dwordx4 v[12:13], v[2:5], off nt
	s_nop 1
	v_or_b32_e32 v2, v70, v82
	v_ashrrev_i32_e32 v3, 31, v2
	v_lshlrev_b64 v[2:3], 11, v[2:3]
	v_lshl_add_u64 v[2:3], v[10:11], 0, v[2:3]
	s_waitcnt lgkmcnt(0)
	global_store_dwordx4 v[2:3], v[6:9], off nt
	v_add_u32_e32 v2, 0x880, v0
	v_add_u32_e32 v4, 0x888, v0
	ds_read2_b32 v[2:3], v2 offset1:1
	ds_read2_b32 v[4:5], v4 offset1:1
	v_or_b32_e32 v6, v70, v83
	v_ashrrev_i32_e32 v7, 31, v6
	v_lshlrev_b64 v[6:7], 11, v[6:7]
	v_lshl_add_u64 v[12:13], v[10:11], 0, v[6:7]
	v_add_u32_e32 v6, 0xcc0, v0
	v_add_u32_e32 v0, 0xcc8, v0
	ds_read2_b32 v[6:7], v6 offset1:1
	ds_read2_b32 v[8:9], v0 offset1:1
	s_waitcnt lgkmcnt(2)
	global_store_dwordx4 v[12:13], v[2:5], off nt
	s_nop 1
	v_or_b32_e32 v2, v70, v84
	v_ashrrev_i32_e32 v3, 31, v2
	v_lshlrev_b64 v[2:3], 11, v[2:3]
	v_lshl_add_u64 v[2:3], v[10:11], 0, v[2:3]
	s_waitcnt lgkmcnt(0)
	global_store_dwordx4 v[2:3], v[6:9], off nt
	s_waitcnt lgkmcnt(0)

; #define LAS __attribute__((address_space(3)))
; __device__ __forceinline__ unsigned pk4_fp8(float a, float b, float c, float d) { unsigned w = 0u; w = __builtin_amdgcn_cvt_pk_fp8_f32(a, b, w, false); w = __builtin_amdgcn_cvt_pk_fp8_f32(c, d, w, true); return w; }
; __device__ __forceinline__ void conv_item8(const float* W, int K, int N, unsigned char* WT, int k0, int n0, int drow0, LAS unsigned* scr, int lane, float sc, bool rperm = false) {
;     const int q = lane >> 4, n4 = lane & 15;
;     f32x4 v[4][4];
; #pragma unroll
;     for (int i = 0; i < 4; ++i)
; #pragma unroll
;         for (int t = 0; t < 4; ++t) v[i][t] = __builtin_nontemporal_load((const f32x4*)(W + (size_t)(k0 + 4 * (4 * i + q) + t) * N + n0 + 4 * n4));
; #pragma unroll
;     for (int i = 0; i < 4; ++i) { const int rp = 4 * i + q; LAS unsigned* sp = scr + (4 * n4) * 17 + rp;
;         sp[0]  = pk4_fp8(v[i][0].x * sc, v[i][1].x * sc, v[i][2].x * sc, v[i][3].x * sc);
;         sp[17] = pk4_fp8(v[i][0].y * sc, v[i][1].y * sc, v[i][2].y * sc, v[i][3].y * sc);
;         sp[34] = pk4_fp8(v[i][0].z * sc, v[i][1].z * sc, v[i][2].z * sc, v[i][3].z * sc);
;         sp[51] = pk4_fp8(v[i][0].w * sc, v[i][1].w * sc, v[i][2].w * sc, v[i][3].w * sc); }
; __device__ __forceinline__ void conv_dispatch(const Params& p, int it, LAS unsigned* scr, int lane) {
;     ...
;     if (r < i_in) { const int N = l ? ODW : EVW, nb = N / 64;
;         conv_item8(p.in[l ? 16 : 5], D, N, l ? p.wp[IX_WIN1] : p.wp[IX_WIN0], (r / nb) * 64, (r % nb) * 64, (r % nb) * 64, scr, lane, F8_SW, l == 1 && (r % nb) < 64 && ((r % nb) & 1) == 0);
.LBB0_167:
	s_andn2_saveexec_b64 s[48:49], s[8:9]
	s_cbranch_execz .LBB0_156
	v_cndmask_b32_e32 v162, 40, v191, vcc
	v_lshl_add_u64 v[2:3], s[0:1], 0, v[162:163]
	global_load_dwordx2 v[2:3], v[2:3], off
	v_cndmask_b32_e32 v20, v196, v197, vcc
	v_lshrrev_b32_e32 v0, 6, v20
	v_sub_u32_e32 v5, 0, v0
	v_max_i32_e32 v5, v0, v5
	v_cvt_f32_u32_e32 v6, v5
	v_sub_u32_e32 v7, 0, v4
	v_cndmask_b32_e32 v162, v198, v199, vcc
	v_max_i32_e32 v8, v4, v7
	v_rcp_iflag_f32_e32 v9, v6
	v_lshl_add_u64 v[6:7], s[0:1], 0, v[162:163]
	global_load_dwordx2 v[72:73], v[6:7], off
	v_sub_u32_e32 v7, 0, v5
	v_mul_f32_e32 v9, 0x4f7ffffe, v9
	v_cvt_u32_f32_e32 v9, v9
	v_xor_b32_e32 v10, v4, v0
	v_ashrrev_i32_e32 v6, 31, v10
	v_lshlrev_b32_e32 v162, 2, v66
	v_mul_lo_u32 v7, v7, v9
	v_mul_hi_u32 v7, v9, v7
	v_add_u32_e32 v7, v9, v7
	v_mul_hi_u32 v7, v8, v7
	v_mul_lo_u32 v9, v7, v5
	v_sub_u32_e32 v8, v8, v9
	v_add_u32_e32 v10, 1, v7
	v_cmp_ge_u32_e64 s[6:7], v8, v5
	v_sub_u32_e32 v9, v8, v5
	v_mov_b32_e32 v92, v163
	v_cndmask_b32_e64 v7, v7, v10, s[6:7]
	v_cndmask_b32_e64 v8, v8, v9, s[6:7]
	v_add_u32_e32 v9, 1, v7
	v_cmp_ge_u32_e64 s[6:7], v8, v5
	v_mov_b32_e32 v93, v163
	v_mov_b32_e32 v75, v163
	v_cndmask_b32_e64 v5, v7, v9, s[6:7]
	v_xor_b32_e32 v5, v5, v6
	v_sub_u32_e32 v5, v5, v6
	v_mul_lo_u32 v0, v5, v0
	v_sub_u32_e32 v22, v4, v0
	v_lshlrev_b32_e32 v74, 6, v5
	v_lshlrev_b32_e32 v70, 6, v22
	v_or_b32_e32 v21, v74, v77
	v_ashrrev_i32_e32 v71, 31, v70
	v_or_b32_e32 v0, 1, v21
	v_or_b32_e32 v8, 2, v21
	v_or_b32_e32 v10, 3, v21
	v_mad_i64_i32 v[4:5], s[6:7], v21, v20, 0
	v_mad_i64_i32 v[6:7], s[6:7], v0, v20, 0
	v_mad_i64_i32 v[8:9], s[6:7], v8, v20, 0
	v_mad_i64_i32 v[10:11], s[6:7], v10, v20, 0
	v_or_b32_e32 v12, 16, v21
	v_or_b32_e32 v13, 17, v21
	v_or_b32_e32 v14, 18, v21
	v_or_b32_e32 v15, 19, v21
	v_and_b32_e32 v30, 1, v22
	v_or_b32_e32 v24, 33, v21
	v_or_b32_e32 v26, 34, v21
	v_or_b32_e32 v28, 35, v21
	v_mad_i64_i32 v[24:25], s[8:9], v24, v20, 0
	v_mad_i64_i32 v[26:27], s[8:9], v26, v20, 0
	v_mad_i64_i32 v[28:29], s[8:9], v28, v20, 0
	v_mov_b32_e32 v0, v163
	v_mov_b32_e32 v87, v163
	s_waitcnt vmcnt(0)
	v_lshl_add_u64 v[2:3], v[70:71], 2, v[2:3]
	v_lshl_add_u64 v[18:19], v[2:3], 0, v[162:163]
	v_lshl_add_u64 v[2:3], v[4:5], 2, v[18:19]
	v_lshl_add_u64 v[4:5], v[6:7], 2, v[18:19]
	v_lshl_add_u64 v[6:7], v[8:9], 2, v[18:19]
	v_lshl_add_u64 v[8:9], v[10:11], 2, v[18:19]
	global_load_dwordx4 v[34:37], v[2:3], off nt
	global_load_dwordx4 v[38:41], v[4:5], off nt
	global_load_dwordx4 v[42:45], v[6:7], off nt
	global_load_dwordx4 v[46:49], v[8:9], off nt
	v_mad_i64_i32 v[2:3], s[6:7], v12, v20, 0
	v_mad_i64_i32 v[4:5], s[6:7], v13, v20, 0
	v_mad_i64_i32 v[6:7], s[6:7], v14, v20, 0
	v_mad_i64_i32 v[8:9], s[6:7], v15, v20, 0
	v_lshl_add_u64 v[2:3], v[2:3], 2, v[18:19]
	v_lshl_add_u64 v[4:5], v[4:5], 2, v[18:19]
	v_lshl_add_u64 v[6:7], v[6:7], 2, v[18:19]
	v_lshl_add_u64 v[8:9], v[8:9], 2, v[18:19]
	global_load_dwordx4 v[10:13], v[2:3], off nt
	global_load_dwordx4 v[14:17], v[4:5], off nt
	s_nop 0
	global_load_dwordx4 v[2:5], v[6:7], off nt
	s_nop 0
	global_load_dwordx4 v[6:9], v[8:9], off nt
	v_cmp_gt_i32_e64 s[6:7], 64, v22
	v_or_b32_e32 v22, 32, v21
	v_mad_i64_i32 v[22:23], s[8:9], v22, v20, 0
	v_lshl_add_u64 v[22:23], v[22:23], 2, v[18:19]
	v_lshl_add_u64 v[24:25], v[24:25], 2, v[18:19]
	v_lshl_add_u64 v[26:27], v[26:27], 2, v[18:19]
	v_lshl_add_u64 v[28:29], v[28:29], 2, v[18:19]
	global_load_dwordx4 v[58:61], v[22:23], off nt
	global_load_dwordx4 v[62:65], v[24:25], off nt
	global_load_dwordx4 v[50:53], v[26:27], off nt
	global_load_dwordx4 v[54:57], v[28:29], off nt
	v_or_b32_e32 v22, 48, v21
	v_or_b32_e32 v24, 49, v21
	v_or_b32_e32 v26, 50, v21
	v_or_b32_e32 v21, 51, v21
	v_mad_i64_i32 v[22:23], s[50:51], v22, v20, 0
	v_mad_i64_i32 v[24:25], s[50:51], v24, v20, 0
	v_mad_i64_i32 v[26:27], s[50:51], v26, v20, 0
	v_mad_i64_i32 v[20:21], s[50:51], v21, v20, 0
	v_lshl_add_u64 v[22:23], v[22:23], 2, v[18:19]
	v_lshl_add_u64 v[24:25], v[24:25], 2, v[18:19]
	v_cmp_eq_u32_e64 s[8:9], 0, v30
	v_lshl_add_u64 v[88:89], v[26:27], 2, v[18:19]
	v_lshl_add_u64 v[90:91], v[20:21], 2, v[18:19]
	global_load_dwordx4 v[26:29], v[22:23], off nt
	global_load_dwordx4 v[30:33], v[24:25], off nt
	global_load_dwordx4 v[18:21], v[88:89], off nt
	s_nop 0
	global_load_dwordx4 v[22:25], v[90:91], off nt
	v_mov_b32_e32 v71, v163
	s_and_b64 s[6:7], s[6:7], s[8:9]
	s_and_b64 vcc, vcc, s[6:7]
	s_waitcnt vmcnt(15)
	v_mul_f32_e32 v34, 0x43800000, v34
	s_waitcnt vmcnt(14)
	v_mul_f32_e32 v38, 0x43800000, v38
	v_mul_f32_e32 v35, 0x43800000, v35
	v_mul_f32_e32 v39, 0x43800000, v39
	v_cvt_pk_fp8_f32 v0, v34, v38
	v_mul_f32_e32 v36, 0x43800000, v36
	v_mul_f32_e32 v40, 0x43800000, v40
	v_cvt_pk_fp8_f32 v71, v35, v39
	v_mul_f32_e32 v37, 0x43800000, v37
	v_mul_f32_e32 v41, 0x43800000, v41
	v_cvt_pk_fp8_f32 v75, v36, v40
	s_waitcnt vmcnt(13)
	v_mul_f32_e32 v42, 0x43800000, v42
	s_waitcnt vmcnt(12)
	v_mul_f32_e32 v46, 0x43800000, v46
	s_waitcnt vmcnt(11)
	v_mul_f32_e32 v10, 0x43800000, v10
	s_waitcnt vmcnt(10)
	v_mul_f32_e32 v14, 0x43800000, v14
	v_mul_f32_e32 v11, 0x43800000, v11
	v_mul_f32_e32 v15, 0x43800000, v15
	v_cvt_pk_fp8_f32 v92, v10, v14
	v_cvt_pk_fp8_f32 v93, v11, v15
	s_waitcnt vmcnt(9)
; #define LAS __attribute__((address_space(3)))
; __device__ __forceinline__ unsigned pk4_fp8(float a, float b, float c, float d) { unsigned w = 0u; w = __builtin_amdgcn_cvt_pk_fp8_f32(a, b, w, false); w = __builtin_amdgcn_cvt_pk_fp8_f32(c, d, w, true); return w; }
; __device__ __forceinline__ void conv_item8(const float* W, int K, int N, unsigned char* WT, int k0, int n0, int drow0, LAS unsigned* scr, int lane, float sc, bool rperm = false) {
;     ...
;     for (int i = 0; i < 4; ++i) { const int rp = 4 * i + q; LAS unsigned* sp = scr + (4 * n4) * 17 + rp;
;         sp[0]  = pk4_fp8(v[i][0].x * sc, v[i][1].x * sc, v[i][2].x * sc, v[i][3].x * sc);
;         sp[17] = pk4_fp8(v[i][0].y * sc, v[i][1].y * sc, v[i][2].y * sc, v[i][3].y * sc);
;         sp[34] = pk4_fp8(v[i][0].z * sc, v[i][1].z * sc, v[i][2].z * sc, v[i][3].z * sc);
;         sp[51] = pk4_fp8(v[i][0].w * sc, v[i][1].w * sc, v[i][2].w * sc, v[i][3].w * sc); }
;     asm volatile("s_waitcnt lgkmcnt(0)" ::: "memory");
;     const int c = lane & 3;
; #pragma unroll
;     for (int j = 0; j < 4; ++j) {
;         const int n = (lane >> 2) + 16 * j; const LAS unsigned* sp = scr + n * 17 + 4 * c;
;         u32x4 o; o.x = sp[0]; o.y = sp[1]; o.z = sp[2]; o.w = sp[3];
;         const int nr = (rperm && n < 32) ? ((n < 16) ? 2 * n : 2 * (n - 16) + 1) : n;
;         *(u32x4*)(WT + (size_t)(drow0 + nr) * K + k0 + 16 * c) = o;
;     }
;     asm volatile("s_waitcnt lgkmcnt(0)" ::: "memory");
	v_mul_f32_e32 v2, 0x43800000, v2
	s_waitcnt vmcnt(8)
	v_mul_f32_e32 v6, 0x43800000, v6
	v_mul_f32_e32 v3, 0x43800000, v3
	v_mul_f32_e32 v7, 0x43800000, v7
	v_mul_f32_e32 v12, 0x43800000, v12
	v_mul_f32_e32 v16, 0x43800000, v16
	v_cvt_pk_fp8_f32 v92, v2, v6 op_sel:[0,0,1]
	v_mul_f32_e32 v2, 0x43800000, v4
	v_mov_b32_e32 v4, v163
	v_cvt_pk_fp8_f32 v93, v3, v7 op_sel:[0,0,1]
	v_mul_f32_e32 v3, 0x43800000, v8
	v_cvt_pk_fp8_f32 v4, v12, v16
	v_mul_f32_e32 v6, 0x43800000, v13
	v_mul_f32_e32 v7, 0x43800000, v17
	v_mov_b32_e32 v8, v163
	v_cvt_pk_fp8_f32 v87, v37, v41
	v_cvt_pk_fp8_f32 v8, v6, v7
	v_mul_f32_e32 v43, 0x43800000, v43
	v_mul_f32_e32 v47, 0x43800000, v47
	v_cvt_pk_fp8_f32 v0, v42, v46 op_sel:[0,0,1]
	v_mul_f32_e32 v44, 0x43800000, v44
	v_mul_f32_e32 v48, 0x43800000, v48
	v_cvt_pk_fp8_f32 v71, v43, v47 op_sel:[0,0,1]
	v_mul_f32_e32 v45, 0x43800000, v45
	v_mul_f32_e32 v49, 0x43800000, v49
	v_cvt_pk_fp8_f32 v75, v44, v48 op_sel:[0,0,1]
	v_cvt_pk_fp8_f32 v4, v2, v3 op_sel:[0,0,1]
	v_mul_f32_e32 v2, 0x43800000, v5
	v_mul_f32_e32 v3, 0x43800000, v9
	v_cvt_pk_fp8_f32 v87, v45, v49 op_sel:[0,0,1]
	v_cvt_pk_fp8_f32 v8, v2, v3 op_sel:[0,0,1]
	ds_write2_b32 v78, v0, v92 offset1:4
	ds_write2_b32 v78, v71, v93 offset0:17 offset1:21
	ds_write2_b32 v78, v75, v4 offset0:34 offset1:38
	ds_write2_b32 v78, v87, v8 offset0:51 offset1:55
	s_waitcnt vmcnt(7)
	v_mul_f32_e32 v0, 0x43800000, v58
	s_waitcnt vmcnt(6)
	v_mul_f32_e32 v2, 0x43800000, v62
	v_mov_b32_e32 v5, v163
	v_cvt_pk_fp8_f32 v5, v0, v2
	v_mul_f32_e32 v0, 0x43800000, v59
	v_mul_f32_e32 v2, 0x43800000, v63
	v_mov_b32_e32 v6, v163
	v_cvt_pk_fp8_f32 v6, v0, v2
	s_waitcnt vmcnt(5)
	v_mul_f32_e32 v0, 0x43800000, v51
	s_waitcnt vmcnt(4)
	v_mul_f32_e32 v2, 0x43800000, v55
	v_mov_b32_e32 v7, v163
	v_cvt_pk_fp8_f32 v6, v0, v2 op_sel:[0,0,1]
	v_mul_f32_e32 v0, 0x43800000, v60
	v_mul_f32_e32 v2, 0x43800000, v64
	v_cvt_pk_fp8_f32 v7, v0, v2
	v_mul_f32_e32 v0, 0x43800000, v61
	v_mul_f32_e32 v2, 0x43800000, v65
	v_mov_b32_e32 v8, v163
	v_cvt_pk_fp8_f32 v8, v0, v2
	v_mul_f32_e32 v0, 0x43800000, v53
	v_mul_f32_e32 v2, 0x43800000, v57
	v_mov_b32_e32 v9, v163
	v_cvt_pk_fp8_f32 v8, v0, v2 op_sel:[0,0,1]
	s_waitcnt vmcnt(3)
	v_mul_f32_e32 v0, 0x43800000, v26
	s_waitcnt vmcnt(2)
	v_mul_f32_e32 v2, 0x43800000, v30
	v_cvt_pk_fp8_f32 v9, v0, v2
	v_mul_f32_e32 v0, 0x43800000, v27
	v_mul_f32_e32 v2, 0x43800000, v31
	v_mov_b32_e32 v10, v163
	v_cvt_pk_fp8_f32 v10, v0, v2
	s_waitcnt vmcnt(1)
	v_mul_f32_e32 v0, 0x43800000, v19
	s_waitcnt vmcnt(0)
	v_mul_f32_e32 v2, 0x43800000, v23
	v_mul_f32_e32 v3, 0x43800000, v50
	v_mul_f32_e32 v4, 0x43800000, v54
	v_cvt_pk_fp8_f32 v10, v0, v2 op_sel:[0,0,1]
	v_mul_f32_e32 v0, 0x43800000, v28
	v_mul_f32_e32 v2, 0x43800000, v32
	v_mov_b32_e32 v11, v163
	v_cvt_pk_fp8_f32 v5, v3, v4 op_sel:[0,0,1]
	v_mul_f32_e32 v3, 0x43800000, v52
	v_mul_f32_e32 v4, 0x43800000, v56
	v_cvt_pk_fp8_f32 v11, v0, v2
	v_mul_f32_e32 v0, 0x43800000, v29
	v_mul_f32_e32 v2, 0x43800000, v33
	v_mov_b32_e32 v12, v163
	v_cvt_pk_fp8_f32 v7, v3, v4 op_sel:[0,0,1]
	v_mul_f32_e32 v3, 0x43800000, v18
	v_mul_f32_e32 v4, 0x43800000, v22
	v_cvt_pk_fp8_f32 v12, v0, v2
	v_cvt_pk_fp8_f32 v9, v3, v4 op_sel:[0,0,1]
	v_mul_f32_e32 v3, 0x43800000, v20
	v_mul_f32_e32 v4, 0x43800000, v24
	v_cvt_pk_fp8_f32 v11, v3, v4 op_sel:[0,0,1]
	v_mul_f32_e32 v0, 0x43800000, v21
	v_mul_f32_e32 v2, 0x43800000, v25
	v_cvt_pk_fp8_f32 v12, v0, v2 op_sel:[0,0,1]
	ds_write2_b32 v78, v5, v9 offset0:8 offset1:12
	ds_write2_b32 v78, v6, v10 offset0:25 offset1:29
	ds_write2_b32 v78, v7, v11 offset0:42 offset1:46
	ds_write2_b32 v78, v8, v12 offset0:59 offset1:63
	v_ashrrev_i32_e32 v75, 31, v74
	s_waitcnt lgkmcnt(0)
	v_lshl_add_u64 v[2:3], v[72:73], 0, v[74:75]
	v_add_u32_e32 v0, v80, v81
	v_lshl_add_u64 v[10:11], v[2:3], 0, v[68:69]
	ds_read2_b32 v[2:3], v0 offset1:1
	ds_read2_b32 v[4:5], v0 offset0:2 offset1:3
	v_cndmask_b32_e64 v6, 0, 1, vcc
	v_lshl_or_b32 v6, v79, v6, v70
	v_ashrrev_i32_e32 v7, 31, v6
	v_lshlrev_b64 v[6:7], 11, v[6:7]
	v_lshl_add_u64 v[12:13], v[10:11], 0, v[6:7]
	v_add_u32_e32 v6, 0x440, v0
	v_add_u32_e32 v8, 0x448, v0
	ds_read2_b32 v[6:7], v6 offset1:1
	ds_read2_b32 v[8:9], v8 offset1:1
	s_waitcnt lgkmcnt(2)
	global_store_dwordx4 v[12:13], v[2:5], off nt
	s_nop 1
	v_cndmask_b32_e32 v2, v82, v85, vcc
	v_or_b32_e32 v2, v2, v70
	v_ashrrev_i32_e32 v3, 31, v2
	v_lshlrev_b64 v[2:3], 11, v[2:3]
	v_lshl_add_u64 v[2:3], v[10:11], 0, v[2:3]
	s_waitcnt lgkmcnt(0)
	global_store_dwordx4 v[2:3], v[6:9], off nt
	v_add_u32_e32 v2, 0x880, v0
	v_add_u32_e32 v4, 0x888, v0
	ds_read2_b32 v[2:3], v2 offset1:1
	ds_read2_b32 v[4:5], v4 offset1:1
	v_or_b32_e32 v6, v70, v83
	v_ashrrev_i32_e32 v7, 31, v6
	v_lshlrev_b64 v[6:7], 11, v[6:7]
	v_lshl_add_u64 v[12:13], v[10:11], 0, v[6:7]
	v_add_u32_e32 v6, 0xcc0, v0
	v_add_u32_e32 v0, 0xcc8, v0
	ds_read2_b32 v[6:7], v6 offset1:1
	ds_read2_b32 v[8:9], v0 offset1:1
	s_waitcnt lgkmcnt(2)
	global_store_dwordx4 v[12:13], v[2:5], off nt
	s_nop 1
	v_or_b32_e32 v2, v70, v84
	v_ashrrev_i32_e32 v3, 31, v2
	v_lshlrev_b64 v[2:3], 11, v[2:3]
	v_lshl_add_u64 v[2:3], v[10:11], 0, v[2:3]
	s_waitcnt lgkmcnt(0)
	global_store_dwordx4 v[2:3], v[6:9], off nt
	s_waitcnt lgkmcnt(0)
	s_branch .LBB0_156
